# DATT softmax: packed f32 subtract and row-sum on top of lazy rescale, rel0 rescale skip, q-conversion in finish tail, WATT/XATT lazy rescale
# speedup vs baseline: 1.0027x; 1.0027x over previous
; #define LAS __attribute__((address_space(3)))
; __device__ __forceinline__ int otid(int wv) { int t = wv * 64 + lane_id(); asm volatile("" : "+v"(t)); return t; }
; template <int PH, bool PRB = false>
; __device__ __forceinline__ void run_phase(int layer, LAS unsigned char* lds, const int wv_) {
;     ...
;     if constexpr (PH == PH_DATT) {
;         float* lse = (float*)(ws + WS_MISC + MISC_LSE);
;         LAS float* tb = (LAS float*)(lds + 132096 + 4096);
;         for (int it = bid; it < 512; it += G) {
;             const bool dbl = it < 256; const int g = dbl ? (it >> 7) : 2, cc = dbl ? (it & 127) : (it - 256), hh = cc & 7, rest = cc >> 3;
;             const int dil = g == 0 ? 1 : (g == 1 ? 4 : 16), r = rest % dil, chunk = rest / dil;
;             { const int t2 = otid(wv); if (t2 < 256) { const int d = t2 - 128; tb[t2] = (d >= -64 && d <= 64) ? bto[(g * 8 + hh) * 129 + d + 64] * 1.4426950408889634f : -__builtin_inff(); } }
;             att::DattRun R{ws + WS_Z, (bf16*)(ws + WS_Z + Z_OB), PRB ? (float*)(ws + WS_H + 26 * MiB) : lse, tb, g, hh, dil, r, chunk * (dbl ? 16 : 8), S / dil, PRB ? y : nullptr, dbl ? 16 : 8};
;             att::datt_stream(lds, R, 0.08838834764831845f * 1.4426950408889634f, wv);
;         }
.LBB0_403:
	s_bitcmp1_b32 s80, 0
	s_cselect_b64 s[2:3], -1, 0
	s_mov_b64 s[0:1], -1
	s_and_b64 vcc, exec, s[2:3]
	v_writelane_b32 v255, s80, 1
	s_waitcnt lgkmcnt(0)
	s_barrier
	s_cbranch_vccz .LBB0_636
	s_mov_b64 s[0:1], 0
	s_mov_b32 s100, 0
	s_mov_b32 s101, 0
	s_mov_b32 s2, s80
	v_mbcnt_lo_u32_b32 v0, -1, 0
	v_mbcnt_hi_u32_b32 v0, -1, v0
	v_readlane_b32 s50, v254, 0
	v_add_u32_e32 v0, s93, v0
	s_cmpk_gt_i32 s50, 0x1ff
	s_cbranch_scc1 .LBB0_524
	v_readlane_b32 s2, v254, 1
	v_readlane_b32 s3, v254, 2
	s_add_u32 s0, s2, s0
	s_addc_u32 s1, s3, s1
	s_load_dwordx2 s[0:1], s[0:1], 0xe0
	s_waitcnt lgkmcnt(0)
	s_add_u32 s2, s0, 0x8100000
	v_writelane_b32 v255, s2, 2
	s_addc_u32 s2, s1, 0
	v_writelane_b32 v255, s2, 3
	s_add_u32 s2, s0, 0x21c00000
	v_writelane_b32 v255, s2, 4
	s_addc_u32 s2, s1, 0
	v_writelane_b32 v255, s2, 5
	s_add_u32 s2, s0, 0x11100000
	v_writelane_b32 v255, s2, 6
	v_writelane_b32 v255, s0, 7
	s_nop 1
	v_writelane_b32 v255, s1, 8
	s_addc_u32 s0, s1, 0
	v_writelane_b32 v255, s0, 9
	s_branch .LBB0_407

; __device__ __forceinline__ void datt_stream(LAS unsigned char* lds, const DattRun& c, const float C, const int wv) {
;     ...
;     auto compute = [&](const int rel, const int b, const int pa) __attribute__((always_inline)) {
;         const int tr = edge ? 0 : (rel == 1 ? 1 : (par ? (rel == 0 ? 2 : 0) : (rel == 2 ? 3 : 0))); const bool do0 = tr != 2, do1 = tr != 3;
;         if (rel == 0) {
; #pragma unroll
;             for (int d0 = 0; d0 < 8; ++d0) qr[d0] = f8tob(qraw[d0]); }
.LBB0_432:
	s_cmp_eq_u32 s101, 3
	s_cbranch_scc0 .Ldatt_qcv0_do
	s_mov_b32 s101, 0
	s_branch .Ldatt_qcv0_done

; #define LAS __attribute__((address_space(3)))
; __device__ __forceinline__ void datt_stream(LAS unsigned char* lds, const DattRun& c, const float C, const int wv) {
;     ...
;         const int tr = edge ? 0 : (rel == 1 ? 1 : (par ? (rel == 0 ? 2 : 0) : (rel == 2 ? 3 : 0))); const bool do0 = tr != 2, do1 = tr != 3;
;         if (rel == 0) {
; #pragma unroll
;             for (int d0 = 0; d0 < 8; ++d0) qr[d0] = f8tob(qraw[d0]); }
;         f32x16 p0, p1;
; #pragma unroll
;         for (int r = 0; r < 16; ++r) { p0[r] = 0.f; p1[r] = 0.f; }
;         const LAS unsigned char* Ks = K_lds + b * SHM_T;
;         if (do0) {
; #pragma unroll
;             for (int d0 = 0; d0 < 8; ++d0) { const bf16x8 b0 = *(const LAS bf16x8*)(Ks + ATT_KSWZ(r32, (d0 * 16 + hi * 8) * 2)); p0 = __builtin_amdgcn_mfma_f32_32x32x16_bf16(b0, qr[d0], p0, 0, 0, 0); } }
.Ldatt_qcv0_done:
	s_cmp_lg_u32 s6, 2
	s_cselect_b64 s[8:9], -1, 0
	s_cmp_eq_u32 s6, 2
	s_cbranch_scc0 .LBB0_430

; __device__ __forceinline__ int crow(int r, int hi) { return (r & 3) + 8 * (r >> 2) + 4 * hi; }
; __device__ __forceinline__ void datt_stream(LAS unsigned char* lds, const DattRun& c, const float C, const int wv) {
;     ...
;         float pmax = -__builtin_inff();
;         if (do0) {
; #pragma unroll
;             for (int r = 0; r < 16; ++r) pmax = fmaxf(pmax, p0[r]); }
;         if (do1) {
; #pragma unroll
;             for (int r = 0; r < 16; ++r) pmax = fmaxf(pmax, p1[r]); }
;         { auto rr = __builtin_amdgcn_permlane32_swap(__float_as_uint(pmax), __float_as_uint(pmax), false, false);
;           pmax = fmaxf(__uint_as_float(rr[0]), __uint_as_float(rr[1])); }
;         const float mn = fmaxf(m_reg, pmax), alpha = __builtin_amdgcn_exp2f(m_reg - mn); m_reg = mn;
;         float ps = 0.f;
;         if (do0) {
; #pragma unroll
;             for (int r = 0; r < 16; ++r) { p0[r] = __builtin_amdgcn_exp2f(p0[r] - mn); ps += p0[r]; } }
;         if (do1) {
; #pragma unroll
;             for (int r = 0; r < 16; ++r) { p1[r] = __builtin_amdgcn_exp2f(p1[r] - mn); ps += p1[r]; } }
;         { auto rr = __builtin_amdgcn_permlane32_swap(__float_as_uint(ps), __float_as_uint(ps), false, false);
;           ps = __uint_as_float(rr[0]) + __uint_as_float(rr[1]); }
;         l_reg = l_reg * alpha + ps;
;         if (__any(alpha < 1.f)) { if (hi == 0) al_l[r32] = alpha; asm volatile("s_waitcnt lgkmcnt(0)" ::: "memory");
; #pragma unroll
;             for (int r = 0; r < 16; ++r) { const float a = al_l[crow(r, hi)];
; #pragma unroll
;                 for (int d = 0; d < 4; ++d) o[d][r] *= a; } }
.LBB0_451:
	v_mov_b32_e32 v98, v64
	s_nop 1
	v_permlane32_swap_b32_e32 v64, v98
	v_max3_f32 v243, v245, v64, v98
	v_sub_f32_e32 v98, v243, v245
	v_cmp_lt_f32_e32 vcc, 0x41000000, v98
	s_cbranch_vccnz .Ldatt_lz0
	v_mov_b32_e32 v243, v245
.Ldatt_lz0:
	s_and_b64 vcc, exec, s[6:7]
	v_mov_b32_e32 v64, 0
	s_cbranch_vccnz .LBB0_453
	v_mov_b32_e32 v98, v243
	v_mov_b32_e32 v99, v243
	v_pk_add_f32 v[82:83], v[82:83], v[98:99] neg_lo:[0,1] neg_hi:[0,1]
	v_pk_add_f32 v[84:85], v[84:85], v[98:99] neg_lo:[0,1] neg_hi:[0,1]
	v_pk_add_f32 v[86:87], v[86:87], v[98:99] neg_lo:[0,1] neg_hi:[0,1]
	v_pk_add_f32 v[88:89], v[88:89], v[98:99] neg_lo:[0,1] neg_hi:[0,1]
	v_pk_add_f32 v[90:91], v[90:91], v[98:99] neg_lo:[0,1] neg_hi:[0,1]
	v_pk_add_f32 v[92:93], v[92:93], v[98:99] neg_lo:[0,1] neg_hi:[0,1]
	v_pk_add_f32 v[94:95], v[94:95], v[98:99] neg_lo:[0,1] neg_hi:[0,1]
	v_pk_add_f32 v[96:97], v[96:97], v[98:99] neg_lo:[0,1] neg_hi:[0,1]
	v_exp_f32_e32 v82, v82
	v_exp_f32_e32 v83, v83
	v_exp_f32_e32 v84, v84
	v_exp_f32_e32 v85, v85
	v_exp_f32_e32 v86, v86
	v_exp_f32_e32 v87, v87
	v_exp_f32_e32 v88, v88
	v_exp_f32_e32 v89, v89
	v_exp_f32_e32 v90, v90
	v_exp_f32_e32 v91, v91
	v_exp_f32_e32 v92, v92
	v_exp_f32_e32 v93, v93
	v_exp_f32_e32 v94, v94
	v_exp_f32_e32 v95, v95
	v_exp_f32_e32 v96, v96
	v_exp_f32_e32 v97, v97
	v_pk_add_f32 v[98:99], v[82:83], v[84:85]
	v_pk_add_f32 v[98:99], v[98:99], v[86:87]
	v_pk_add_f32 v[98:99], v[98:99], v[88:89]
	v_pk_add_f32 v[98:99], v[98:99], v[90:91]
	v_pk_add_f32 v[98:99], v[98:99], v[92:93]
	v_pk_add_f32 v[98:99], v[98:99], v[94:95]
	v_pk_add_f32 v[98:99], v[98:99], v[96:97]
	v_add_f32_e32 v64, v98, v99
.LBB0_453:
	s_and_b64 vcc, exec, s[8:9]
	s_cbranch_vccnz .LBB0_455
	v_mov_b32_e32 v98, v243
	v_mov_b32_e32 v99, v243
	v_pk_add_f32 v[66:67], v[66:67], v[98:99] neg_lo:[0,1] neg_hi:[0,1]
	v_pk_add_f32 v[68:69], v[68:69], v[98:99] neg_lo:[0,1] neg_hi:[0,1]
	v_pk_add_f32 v[70:71], v[70:71], v[98:99] neg_lo:[0,1] neg_hi:[0,1]
	v_pk_add_f32 v[72:73], v[72:73], v[98:99] neg_lo:[0,1] neg_hi:[0,1]
	v_pk_add_f32 v[74:75], v[74:75], v[98:99] neg_lo:[0,1] neg_hi:[0,1]
	v_pk_add_f32 v[76:77], v[76:77], v[98:99] neg_lo:[0,1] neg_hi:[0,1]
	v_pk_add_f32 v[78:79], v[78:79], v[98:99] neg_lo:[0,1] neg_hi:[0,1]
	v_pk_add_f32 v[80:81], v[80:81], v[98:99] neg_lo:[0,1] neg_hi:[0,1]
	v_exp_f32_e32 v66, v66
	v_exp_f32_e32 v67, v67
	v_exp_f32_e32 v68, v68
	v_exp_f32_e32 v69, v69
	v_exp_f32_e32 v70, v70
	v_exp_f32_e32 v71, v71
	v_exp_f32_e32 v72, v72
	v_exp_f32_e32 v73, v73
	v_exp_f32_e32 v74, v74
	v_exp_f32_e32 v75, v75
	v_exp_f32_e32 v76, v76
	v_exp_f32_e32 v77, v77
	v_exp_f32_e32 v78, v78
	v_exp_f32_e32 v79, v79
	v_exp_f32_e32 v80, v80
	v_exp_f32_e32 v81, v81
	v_pk_add_f32 v[98:99], v[66:67], v[68:69]
	v_pk_add_f32 v[98:99], v[98:99], v[70:71]
	v_pk_add_f32 v[98:99], v[98:99], v[72:73]
	v_pk_add_f32 v[98:99], v[98:99], v[74:75]
	v_pk_add_f32 v[98:99], v[98:99], v[76:77]
	v_pk_add_f32 v[98:99], v[98:99], v[78:79]
	v_pk_add_f32 v[98:99], v[98:99], v[80:81]
	v_add_f32_e32 v98, v98, v99
	v_add_f32_e32 v64, v98, v64
.LBB0_455:
	v_sub_f32_e32 v98, v245, v243
	v_exp_f32_e32 v245, v98
	v_mov_b32_e32 v244, v64
	s_nop 1
	v_permlane32_swap_b32_e32 v64, v244
	s_cmp_eq_u32 s62, 0
	s_cbranch_scc1 .LBB0_459
	v_cmp_gt_f32_e32 vcc, 1.0, v245
	s_cbranch_vccz .LBB0_459
	s_and_saveexec_b64 s[0:1], s[4:5]
	ds_write_b32 v229, v245 offset:128
	s_or_b64 exec, exec, s[0:1]
	s_waitcnt lgkmcnt(0)
	v_add_u32_e32 v110, s60, v230
	ds_read_b128 v[98:101], v110 offset:224
	ds_read_b128 v[102:105], v110 offset:192
	ds_read_b128 v[106:109], v110 offset:160
	ds_read_b128 v[110:113], v110 offset:128
	s_waitcnt lgkmcnt(3)
	v_pk_mul_f32 v[12:13], v[12:13], v[98:99]
	s_waitcnt lgkmcnt(2)
	v_pk_mul_f32 v[8:9], v[8:9], v[102:103]
	s_waitcnt lgkmcnt(1)
	v_pk_mul_f32 v[4:5], v[4:5], v[106:107]
	v_pk_mul_f32 v[14:15], v[14:15], v[100:101]
	v_pk_mul_f32 v[10:11], v[10:11], v[104:105]
	v_pk_mul_f32 v[6:7], v[6:7], v[108:109]
	s_waitcnt lgkmcnt(0)
	v_pk_mul_f32 v[2:3], v[2:3], v[112:113]
	v_pk_mul_f32 v[0:1], v[0:1], v[110:111]
	v_pk_mul_f32 v[28:29], v[28:29], v[98:99]
	v_pk_mul_f32 v[24:25], v[24:25], v[102:103]
	v_pk_mul_f32 v[20:21], v[20:21], v[106:107]
	v_pk_mul_f32 v[30:31], v[30:31], v[100:101]
	v_pk_mul_f32 v[26:27], v[26:27], v[104:105]
	v_pk_mul_f32 v[22:23], v[22:23], v[108:109]
	v_pk_mul_f32 v[18:19], v[18:19], v[112:113]
	v_pk_mul_f32 v[16:17], v[16:17], v[110:111]
	v_pk_mul_f32 v[44:45], v[44:45], v[98:99]
	v_pk_mul_f32 v[40:41], v[40:41], v[102:103]
	v_pk_mul_f32 v[36:37], v[36:37], v[106:107]
	v_pk_mul_f32 v[46:47], v[46:47], v[100:101]
	v_pk_mul_f32 v[42:43], v[42:43], v[104:105]
	v_pk_mul_f32 v[38:39], v[38:39], v[108:109]
	v_pk_mul_f32 v[34:35], v[34:35], v[112:113]
	v_pk_mul_f32 v[32:33], v[32:33], v[110:111]
	v_pk_mul_f32 v[60:61], v[60:61], v[98:99]
	v_pk_mul_f32 v[56:57], v[56:57], v[102:103]
	v_pk_mul_f32 v[52:53], v[52:53], v[106:107]
	v_pk_mul_f32 v[62:63], v[62:63], v[100:101]
	v_pk_mul_f32 v[58:59], v[58:59], v[104:105]
	v_pk_mul_f32 v[54:55], v[54:55], v[108:109]
	v_pk_mul_f32 v[50:51], v[50:51], v[112:113]
	v_pk_mul_f32 v[48:49], v[48:49], v[110:111]

; #define DS_LOAD(X, s) do { const int _s = (s) < NS - 1 ? (s) : NS - 1; const int _j = 64 * (c.a0 - 1 + _s) + sr; const unsigned _k0 = DS_KROW(_j) + (unsigned)sc, _k1 = DS_KROW(_j + 32) + (unsigned)sc; \
;         ks##X##0 = *(const u32x2*)(zb + _k0); vs##X##0 = *(const u32x2*)(zb + (_k0 + 1024u)); ks##X##1 = *(const u32x2*)(zb + _k1); vs##X##1 = *(const u32x2*)(zb + (_k1 + 1024u)); } while (0)
; #define DS_WRITE(X, b) do { *(LAS bf16x8*)(V_lds + (b) * SHM_T + vst0) = f8tob(vs##X##0); *(LAS bf16x8*)(K_lds + (b) * SHM_T + kst0) = f8tob(ks##X##0); \
;         *(LAS bf16x8*)(V_lds + (b) * SHM_T + vst1) = f8tob(vs##X##1); *(LAS bf16x8*)(K_lds + (b) * SHM_T + kst1) = f8tob(ks##X##1); } while (0)
; #define DS_LOADQ(pa) do { const unsigned _q = roff(64 * (c.a0 + (pa)) + 32 * par + r32) + (unsigned)hi * 8u; _Pragma("unroll") for (int d0 = 0; d0 < 8; ++d0) qraw[d0] = *(const u32x2*)(zb + (_q + d0 * 16u)); } while (0)
; #define DS_RESET() do { m_reg = -1e30f; l_reg = 0.f; _Pragma("unroll") for (int d = 0; d < 4; ++d) _Pragma("unroll") for (int r = 0; r < 16; ++r) o[d][r] = 0.f; } while (0)
; __device__ __forceinline__ void datt_stream(LAS unsigned char* lds, const DattRun& c, const float C, const int wv) {
;     ...
;     bf16x8 qr[8]; u32x2 qraw[8]; float m_reg = -1e30f, l_reg = 0.f; f32x16 o[4];
;     ...
;             if (act && rel <= 2) { compute(rel, q, pa); if (rel == 2 && pa + 4 < NP) DS_LOADQ(pa + 4); }
;             else if (act) { finish(pa); DS_RESET(); }
;             if (q == 0) { DS_WRITE(A, 1); DS_LOAD(A, st + 3); } else { DS_WRITE(B, 0); DS_LOAD(B, st + 3); }
.LBB0_467:
	s_waitcnt vmcnt(4)
	v_cvt_pk_f32_fp8_e32 v[0:1], v206
	v_cvt_pk_f32_fp8_sdwa v[2:3], v206 src0_sel:WORD_1
	v_cvt_pk_f32_fp8_e32 v[4:5], v207
	v_cvt_pk_f32_fp8_sdwa v[6:7], v207 src0_sel:WORD_1
	v_cvt_pk_bf16_f32 v0, v0, v1
	v_cvt_pk_bf16_f32 v1, v2, v3
	v_cvt_pk_bf16_f32 v2, v4, v5
	v_cvt_pk_bf16_f32 v3, v6, v7
	ds_write_b128 v225, v[0:3] offset:16384
	s_waitcnt vmcnt(4)
	v_cvt_pk_f32_fp8_e32 v[0:1], v202
	v_cvt_pk_f32_fp8_sdwa v[2:3], v202 src0_sel:WORD_1
	v_cvt_pk_f32_fp8_e32 v[4:5], v203
	v_cvt_pk_f32_fp8_sdwa v[6:7], v203 src0_sel:WORD_1
	v_cvt_pk_bf16_f32 v0, v0, v1
	v_cvt_pk_bf16_f32 v1, v2, v3
	v_cvt_pk_bf16_f32 v2, v4, v5
	v_cvt_pk_bf16_f32 v3, v6, v7
	ds_write_b128 v226, v[0:3] offset:49152
	s_waitcnt vmcnt(4)
	v_cvt_pk_f32_fp8_e32 v[0:1], v198
	v_cvt_pk_f32_fp8_sdwa v[2:3], v198 src0_sel:WORD_1
	v_cvt_pk_f32_fp8_e32 v[4:5], v199
	v_cvt_pk_f32_fp8_sdwa v[6:7], v199 src0_sel:WORD_1
	v_cvt_pk_bf16_f32 v0, v0, v1
	v_cvt_pk_bf16_f32 v1, v2, v3
	v_cvt_pk_bf16_f32 v2, v4, v5
	v_cvt_pk_bf16_f32 v3, v6, v7
	s_add_i32 s0, s57, 3
	ds_write_b128 v227, v[0:3] offset:16384
	s_waitcnt vmcnt(4)
	v_cvt_pk_f32_fp8_e32 v[0:1], v194
	v_cvt_pk_f32_fp8_sdwa v[2:3], v194 src0_sel:WORD_1
	v_cvt_pk_f32_fp8_e32 v[4:5], v195
	s_min_i32 s0, s0, s81
	v_cvt_pk_f32_fp8_sdwa v[6:7], v195 src0_sel:WORD_1
	v_cvt_pk_bf16_f32 v0, v0, v1
	v_cvt_pk_bf16_f32 v1, v2, v3
	v_cvt_pk_bf16_f32 v2, v4, v5
	v_add_u32_e32 v4, s0, v224
	v_cvt_pk_bf16_f32 v3, v6, v7
	v_lshl_add_u32 v6, v4, 6, v197
	v_add_u32_e32 v4, 32, v6
	v_min_i32_e32 v4, s95, v4
	v_cmp_lt_i32_e32 vcc, s43, v6
	v_min_i32_e32 v7, s95, v6
	s_cmp_gt_u32 s57, s61
	v_cndmask_b32_e32 v4, 0, v4, vcc
	v_cmp_lt_i32_e32 vcc, -1, v6
	v_lshlrev_b32_e32 v4, s45, v4
	v_add_u32_e32 v4, s56, v4
	v_cndmask_b32_e32 v6, 0, v7, vcc
	v_lshlrev_b32_e32 v6, s45, v6
	v_mad_u64_u32 v[4:5], s[0:1], v4, s42, v[196:197]
	v_add_u32_e32 v6, s56, v6
	v_add_u32_e32 v5, 0x400, v4
	v_mad_u64_u32 v[6:7], s[0:1], v6, s42, v[196:197]
	v_add_u32_e32 v7, 0x400, v6
	global_load_dwordx2 v[198:199], v5, s[92:93]
	global_load_dwordx2 v[206:207], v7, s[92:93]
	global_load_dwordx2 v[202:203], v6, s[92:93]
	global_load_dwordx2 v[194:195], v4, s[92:93]
	s_cselect_b64 s[0:1], -1, 0
	s_and_b64 vcc, exec, s[0:1]
	ds_write_b128 v228, v[0:3] offset:49152
	s_cmp_eq_u32 s101, 2
	s_cbranch_scc0 .Ldatt_qc0_skip
	v_cvt_pk_f32_fp8_e32 v[0:1], v176
	v_cvt_pk_f32_fp8_sdwa v[2:3], v176 src0_sel:WORD_1
	v_cvt_pk_f32_fp8_e32 v[4:5], v177
	v_cvt_pk_f32_fp8_sdwa v[6:7], v177 src0_sel:WORD_1
	v_cvt_pk_bf16_f32 v144, v0, v1
	v_cvt_pk_bf16_f32 v145, v2, v3
	v_cvt_pk_bf16_f32 v146, v4, v5
	v_cvt_pk_bf16_f32 v147, v6, v7
	v_cvt_pk_f32_fp8_e32 v[0:1], v178
	v_cvt_pk_f32_fp8_sdwa v[2:3], v178 src0_sel:WORD_1
	v_cvt_pk_f32_fp8_e32 v[4:5], v179
	v_cvt_pk_f32_fp8_sdwa v[6:7], v179 src0_sel:WORD_1
	v_cvt_pk_bf16_f32 v148, v0, v1
	v_cvt_pk_bf16_f32 v149, v2, v3
	v_cvt_pk_bf16_f32 v150, v4, v5
	v_cvt_pk_bf16_f32 v151, v6, v7
	v_cvt_pk_f32_fp8_e32 v[0:1], v180
	v_cvt_pk_f32_fp8_sdwa v[2:3], v180 src0_sel:WORD_1
	v_cvt_pk_f32_fp8_e32 v[4:5], v181
	v_cvt_pk_f32_fp8_sdwa v[6:7], v181 src0_sel:WORD_1
	v_cvt_pk_bf16_f32 v152, v0, v1
	v_cvt_pk_bf16_f32 v153, v2, v3
	v_cvt_pk_bf16_f32 v154, v4, v5
	v_cvt_pk_bf16_f32 v155, v6, v7
	v_cvt_pk_f32_fp8_e32 v[0:1], v182
	v_cvt_pk_f32_fp8_sdwa v[2:3], v182 src0_sel:WORD_1
	v_cvt_pk_f32_fp8_e32 v[4:5], v183
	v_cvt_pk_f32_fp8_sdwa v[6:7], v183 src0_sel:WORD_1
	v_cvt_pk_bf16_f32 v156, v0, v1
	v_cvt_pk_bf16_f32 v157, v2, v3
	v_cvt_pk_bf16_f32 v158, v4, v5
	v_cvt_pk_bf16_f32 v159, v6, v7
	v_cvt_pk_f32_fp8_e32 v[0:1], v184
	v_cvt_pk_f32_fp8_sdwa v[2:3], v184 src0_sel:WORD_1
	v_cvt_pk_f32_fp8_e32 v[4:5], v185
	v_cvt_pk_f32_fp8_sdwa v[6:7], v185 src0_sel:WORD_1
	v_cvt_pk_bf16_f32 v160, v0, v1
	v_cvt_pk_bf16_f32 v161, v2, v3
	v_cvt_pk_bf16_f32 v162, v4, v5
	v_cvt_pk_bf16_f32 v163, v6, v7
	v_cvt_pk_f32_fp8_e32 v[0:1], v188
	v_cvt_pk_f32_fp8_sdwa v[2:3], v188 src0_sel:WORD_1
	v_cvt_pk_f32_fp8_e32 v[4:5], v189
	v_cvt_pk_f32_fp8_sdwa v[6:7], v189 src0_sel:WORD_1
	v_cvt_pk_bf16_f32 v164, v0, v1
	v_cvt_pk_bf16_f32 v165, v2, v3
	v_cvt_pk_bf16_f32 v166, v4, v5
	v_cvt_pk_bf16_f32 v167, v6, v7
	v_cvt_pk_f32_fp8_e32 v[0:1], v190
	v_cvt_pk_f32_fp8_sdwa v[2:3], v190 src0_sel:WORD_1
	v_cvt_pk_f32_fp8_e32 v[4:5], v191
	v_cvt_pk_f32_fp8_sdwa v[6:7], v191 src0_sel:WORD_1
	v_cvt_pk_bf16_f32 v168, v0, v1
	v_cvt_pk_bf16_f32 v169, v2, v3
	v_cvt_pk_bf16_f32 v170, v4, v5
	v_cvt_pk_bf16_f32 v171, v6, v7
	v_cvt_pk_f32_fp8_e32 v[0:1], v192
	v_cvt_pk_f32_fp8_sdwa v[2:3], v192 src0_sel:WORD_1
	v_cvt_pk_f32_fp8_e32 v[4:5], v193
	v_cvt_pk_f32_fp8_sdwa v[6:7], v193 src0_sel:WORD_1
	v_cvt_pk_bf16_f32 v172, v0, v1
	v_cvt_pk_bf16_f32 v173, v2, v3
	v_cvt_pk_bf16_f32 v174, v4, v5
	v_cvt_pk_bf16_f32 v175, v6, v7
	s_mov_b32 s101, 3
.Ldatt_qc0_skip:
	s_cmp_eq_u32 s100, 0
	s_cbranch_scc1 .Ldatt_q0_skip
	s_mov_b32 s100, 0
	s_mov_b32 s101, 2
	global_load_dwordx2 v[176:177], v76, s[92:93]
	global_load_dwordx2 v[178:179], v76, s[92:93] offset:16
	global_load_dwordx2 v[180:181], v76, s[92:93] offset:32
	global_load_dwordx2 v[182:183], v76, s[92:93] offset:48
	global_load_dwordx2 v[184:185], v76, s[92:93] offset:64
	global_load_dwordx2 v[188:189], v76, s[92:93] offset:80
	global_load_dwordx2 v[190:191], v76, s[92:93] offset:96
	global_load_dwordx2 v[192:193], v76, s[92:93] offset:112

; __device__ __forceinline__ void datt_stream(LAS unsigned char* lds, const DattRun& c, const float C, const int wv) {
;     ...
;     auto compute = [&](const int rel, const int b, const int pa) __attribute__((always_inline)) {
;         const int tr = edge ? 0 : (rel == 1 ? 1 : (par ? (rel == 0 ? 2 : 0) : (rel == 2 ? 3 : 0))); const bool do0 = tr != 2, do1 = tr != 3;
;         if (rel == 0) {
; #pragma unroll
;             for (int d0 = 0; d0 < 8; ++d0) qr[d0] = f8tob(qraw[d0]); }
.LBB0_483:
	s_cmp_lg_u32 s63, 0
	s_cbranch_scc1 .LBB0_485
	s_cmp_eq_u32 s101, 3
	s_cbranch_scc0 .Ldatt_qcv1_do
	s_mov_b32 s101, 0
	s_branch .LBB0_485
.Ldatt_qcv1_do:
	v_cvt_pk_f32_fp8_e32 v[0:1], v176
	v_cvt_pk_f32_fp8_sdwa v[2:3], v176 src0_sel:WORD_1
	v_cvt_pk_f32_fp8_e32 v[4:5], v177
	v_cvt_pk_f32_fp8_sdwa v[6:7], v177 src0_sel:WORD_1
	v_cvt_pk_bf16_f32 v144, v0, v1
	v_cvt_pk_bf16_f32 v145, v2, v3
	v_cvt_pk_bf16_f32 v146, v4, v5
	v_cvt_pk_bf16_f32 v147, v6, v7
	v_cvt_pk_f32_fp8_e32 v[0:1], v178
	v_cvt_pk_f32_fp8_sdwa v[2:3], v178 src0_sel:WORD_1
	v_cvt_pk_f32_fp8_e32 v[4:5], v179
	v_cvt_pk_f32_fp8_sdwa v[6:7], v179 src0_sel:WORD_1
	v_cvt_pk_bf16_f32 v148, v0, v1
	v_cvt_pk_bf16_f32 v149, v2, v3
	v_cvt_pk_bf16_f32 v150, v4, v5
	v_cvt_pk_bf16_f32 v151, v6, v7
	v_cvt_pk_f32_fp8_e32 v[0:1], v180
	v_cvt_pk_f32_fp8_sdwa v[2:3], v180 src0_sel:WORD_1
	v_cvt_pk_f32_fp8_e32 v[4:5], v181
	v_cvt_pk_f32_fp8_sdwa v[6:7], v181 src0_sel:WORD_1
	v_cvt_pk_bf16_f32 v152, v0, v1
	v_cvt_pk_bf16_f32 v153, v2, v3
	v_cvt_pk_bf16_f32 v154, v4, v5
	v_cvt_pk_bf16_f32 v155, v6, v7
	v_cvt_pk_f32_fp8_e32 v[0:1], v182
	v_cvt_pk_f32_fp8_sdwa v[2:3], v182 src0_sel:WORD_1
	v_cvt_pk_f32_fp8_e32 v[4:5], v183
	v_cvt_pk_f32_fp8_sdwa v[6:7], v183 src0_sel:WORD_1
	v_cvt_pk_bf16_f32 v156, v0, v1
	v_cvt_pk_bf16_f32 v157, v2, v3
	v_cvt_pk_bf16_f32 v158, v4, v5
	v_cvt_pk_bf16_f32 v159, v6, v7
	s_waitcnt vmcnt(7)
	v_cvt_pk_f32_fp8_e32 v[0:1], v184
	v_cvt_pk_f32_fp8_sdwa v[2:3], v184 src0_sel:WORD_1
	v_cvt_pk_f32_fp8_e32 v[4:5], v185
	v_cvt_pk_f32_fp8_sdwa v[6:7], v185 src0_sel:WORD_1
	v_cvt_pk_bf16_f32 v160, v0, v1
	v_cvt_pk_bf16_f32 v161, v2, v3
	v_cvt_pk_bf16_f32 v162, v4, v5
	v_cvt_pk_bf16_f32 v163, v6, v7
	s_waitcnt vmcnt(6)
	v_cvt_pk_f32_fp8_e32 v[0:1], v188
	v_cvt_pk_f32_fp8_sdwa v[2:3], v188 src0_sel:WORD_1
	v_cvt_pk_f32_fp8_e32 v[4:5], v189
	v_cvt_pk_f32_fp8_sdwa v[6:7], v189 src0_sel:WORD_1
	v_cvt_pk_bf16_f32 v164, v0, v1
	v_cvt_pk_bf16_f32 v165, v2, v3
	v_cvt_pk_bf16_f32 v166, v4, v5
	v_cvt_pk_bf16_f32 v167, v6, v7
	s_waitcnt vmcnt(5)
	v_cvt_pk_f32_fp8_e32 v[0:1], v190
	v_cvt_pk_f32_fp8_sdwa v[2:3], v190 src0_sel:WORD_1
	v_cvt_pk_f32_fp8_e32 v[4:5], v191
	v_cvt_pk_f32_fp8_sdwa v[6:7], v191 src0_sel:WORD_1
	v_cvt_pk_bf16_f32 v168, v0, v1
	v_cvt_pk_bf16_f32 v169, v2, v3
	v_cvt_pk_bf16_f32 v170, v4, v5
	v_cvt_pk_bf16_f32 v171, v6, v7
	s_waitcnt vmcnt(4)
	v_cvt_pk_f32_fp8_e32 v[0:1], v192
	v_cvt_pk_f32_fp8_sdwa v[2:3], v192 src0_sel:WORD_1
	v_cvt_pk_f32_fp8_e32 v[4:5], v193
	v_cvt_pk_f32_fp8_sdwa v[6:7], v193 src0_sel:WORD_1
	v_cvt_pk_bf16_f32 v172, v0, v1
	v_cvt_pk_bf16_f32 v173, v2, v3
	v_cvt_pk_bf16_f32 v174, v4, v5
	v_cvt_pk_bf16_f32 v175, v6, v7

; __device__ __forceinline__ int crow(int r, int hi) { return (r & 3) + 8 * (r >> 2) + 4 * hi; }
; __device__ __forceinline__ void datt_stream(LAS unsigned char* lds, const DattRun& c, const float C, const int wv) {
;     ...
;         float pmax = -__builtin_inff();
;         if (do0) {
; #pragma unroll
;             for (int r = 0; r < 16; ++r) pmax = fmaxf(pmax, p0[r]); }
;         if (do1) {
; #pragma unroll
;             for (int r = 0; r < 16; ++r) pmax = fmaxf(pmax, p1[r]); }
;         { auto rr = __builtin_amdgcn_permlane32_swap(__float_as_uint(pmax), __float_as_uint(pmax), false, false);
;           pmax = fmaxf(__uint_as_float(rr[0]), __uint_as_float(rr[1])); }
;         const float mn = fmaxf(m_reg, pmax), alpha = __builtin_amdgcn_exp2f(m_reg - mn); m_reg = mn;
;         float ps = 0.f;
;         if (do0) {
; #pragma unroll
;             for (int r = 0; r < 16; ++r) { p0[r] = __builtin_amdgcn_exp2f(p0[r] - mn); ps += p0[r]; } }
;         if (do1) {
; #pragma unroll
;             for (int r = 0; r < 16; ++r) { p1[r] = __builtin_amdgcn_exp2f(p1[r] - mn); ps += p1[r]; } }
;         { auto rr = __builtin_amdgcn_permlane32_swap(__float_as_uint(ps), __float_as_uint(ps), false, false);
;           ps = __uint_as_float(rr[0]) + __uint_as_float(rr[1]); }
;         l_reg = l_reg * alpha + ps;
;         if (__any(alpha < 1.f)) { if (hi == 0) al_l[r32] = alpha; asm volatile("s_waitcnt lgkmcnt(0)" ::: "memory");
; #pragma unroll
;             for (int r = 0; r < 16; ++r) { const float a = al_l[crow(r, hi)];
; #pragma unroll
;                 for (int d = 0; d < 4; ++d) o[d][r] *= a; } }
.LBB0_507:
	v_mov_b32_e32 v33, v32
	s_nop 1
	v_permlane32_swap_b32_e32 v32, v33
	v_max3_f32 v245, v243, v32, v33
	v_sub_f32_e32 v33, v245, v243
	v_cmp_lt_f32_e32 vcc, 0x41000000, v33
	s_cbranch_vccnz .Ldatt_lz1
	v_mov_b32_e32 v245, v243
.Ldatt_lz1:
	s_and_b64 vcc, exec, s[6:7]
	v_mov_b32_e32 v64, 0
	s_cbranch_vccnz .LBB0_509
	v_mov_b32_e32 v32, v245
	v_mov_b32_e32 v33, v245
	v_pk_add_f32 v[16:17], v[16:17], v[32:33] neg_lo:[0,1] neg_hi:[0,1]
	v_pk_add_f32 v[18:19], v[18:19], v[32:33] neg_lo:[0,1] neg_hi:[0,1]
	v_pk_add_f32 v[20:21], v[20:21], v[32:33] neg_lo:[0,1] neg_hi:[0,1]
	v_pk_add_f32 v[22:23], v[22:23], v[32:33] neg_lo:[0,1] neg_hi:[0,1]
	v_pk_add_f32 v[24:25], v[24:25], v[32:33] neg_lo:[0,1] neg_hi:[0,1]
	v_pk_add_f32 v[26:27], v[26:27], v[32:33] neg_lo:[0,1] neg_hi:[0,1]
	v_pk_add_f32 v[28:29], v[28:29], v[32:33] neg_lo:[0,1] neg_hi:[0,1]
	v_pk_add_f32 v[30:31], v[30:31], v[32:33] neg_lo:[0,1] neg_hi:[0,1]
	v_exp_f32_e32 v16, v16
	v_exp_f32_e32 v17, v17
	v_exp_f32_e32 v18, v18
	v_exp_f32_e32 v19, v19
	v_exp_f32_e32 v20, v20
	v_exp_f32_e32 v21, v21
	v_exp_f32_e32 v22, v22
	v_exp_f32_e32 v23, v23
	v_exp_f32_e32 v24, v24
	v_exp_f32_e32 v25, v25
	v_exp_f32_e32 v26, v26
	v_exp_f32_e32 v27, v27
	v_exp_f32_e32 v28, v28
	v_exp_f32_e32 v29, v29
	v_exp_f32_e32 v30, v30
	v_exp_f32_e32 v31, v31
	v_pk_add_f32 v[32:33], v[16:17], v[18:19]
	v_pk_add_f32 v[32:33], v[32:33], v[20:21]
	v_pk_add_f32 v[32:33], v[32:33], v[22:23]
	v_pk_add_f32 v[32:33], v[32:33], v[24:25]
	v_pk_add_f32 v[32:33], v[32:33], v[26:27]
	v_pk_add_f32 v[32:33], v[32:33], v[28:29]
	v_pk_add_f32 v[32:33], v[32:33], v[30:31]
	v_add_f32_e32 v64, v32, v33
.LBB0_509:
	s_and_b64 vcc, exec, s[8:9]
	s_cbranch_vccnz .LBB0_511
	v_mov_b32_e32 v32, v245
	v_mov_b32_e32 v33, v245
	v_pk_add_f32 v[0:1], v[0:1], v[32:33] neg_lo:[0,1] neg_hi:[0,1]
	v_pk_add_f32 v[2:3], v[2:3], v[32:33] neg_lo:[0,1] neg_hi:[0,1]
	v_pk_add_f32 v[4:5], v[4:5], v[32:33] neg_lo:[0,1] neg_hi:[0,1]
	v_pk_add_f32 v[6:7], v[6:7], v[32:33] neg_lo:[0,1] neg_hi:[0,1]
	v_pk_add_f32 v[8:9], v[8:9], v[32:33] neg_lo:[0,1] neg_hi:[0,1]
	v_pk_add_f32 v[10:11], v[10:11], v[32:33] neg_lo:[0,1] neg_hi:[0,1]
	v_pk_add_f32 v[12:13], v[12:13], v[32:33] neg_lo:[0,1] neg_hi:[0,1]
	v_pk_add_f32 v[14:15], v[14:15], v[32:33] neg_lo:[0,1] neg_hi:[0,1]
	v_exp_f32_e32 v0, v0
	v_exp_f32_e32 v1, v1
	v_exp_f32_e32 v2, v2
	v_exp_f32_e32 v3, v3
	v_exp_f32_e32 v4, v4
	v_exp_f32_e32 v5, v5
	v_exp_f32_e32 v6, v6
	v_exp_f32_e32 v7, v7
	v_exp_f32_e32 v8, v8
	v_exp_f32_e32 v9, v9
	v_exp_f32_e32 v10, v10
	v_exp_f32_e32 v11, v11
	v_exp_f32_e32 v12, v12
	v_exp_f32_e32 v13, v13
	v_exp_f32_e32 v14, v14
	v_exp_f32_e32 v15, v15
	v_pk_add_f32 v[32:33], v[0:1], v[2:3]
	v_pk_add_f32 v[32:33], v[32:33], v[4:5]
	v_pk_add_f32 v[32:33], v[32:33], v[6:7]
	v_pk_add_f32 v[32:33], v[32:33], v[8:9]
	v_pk_add_f32 v[32:33], v[32:33], v[10:11]
	v_pk_add_f32 v[32:33], v[32:33], v[12:13]
	v_pk_add_f32 v[32:33], v[32:33], v[14:15]
	v_add_f32_e32 v32, v32, v33
	v_add_f32_e32 v64, v32, v64
.LBB0_511:
	v_sub_f32_e32 v32, v243, v245
	v_exp_f32_e32 v66, v32
	v_mov_b32_e32 v67, v64
	s_nop 1
	v_permlane32_swap_b32_e32 v64, v67
	s_cmp_eq_u32 s63, 0
	s_cbranch_scc1 .LBB0_515
	v_cmp_gt_f32_e32 vcc, 1.0, v66
	s_cbranch_vccz .LBB0_515
	s_and_saveexec_b64 s[10:11], s[4:5]
	ds_write_b32 v229, v66 offset:128
	s_or_b64 exec, exec, s[10:11]
	s_waitcnt lgkmcnt(0)
	v_add_u32_e32 v44, s60, v230
	ds_read_b128 v[32:35], v44 offset:224
	ds_read_b128 v[36:39], v44 offset:192
	ds_read_b128 v[40:43], v44 offset:160
	ds_read_b128 v[44:47], v44 offset:128
	s_waitcnt lgkmcnt(3)
	v_pk_mul_f32 v[92:93], v[92:93], v[32:33]
	s_waitcnt lgkmcnt(2)
	v_pk_mul_f32 v[88:89], v[88:89], v[36:37]
	s_waitcnt lgkmcnt(1)
	v_pk_mul_f32 v[84:85], v[84:85], v[40:41]
	v_pk_mul_f32 v[94:95], v[94:95], v[34:35]
	v_pk_mul_f32 v[90:91], v[90:91], v[38:39]
	v_pk_mul_f32 v[86:87], v[86:87], v[42:43]
	s_waitcnt lgkmcnt(0)
	v_pk_mul_f32 v[82:83], v[82:83], v[46:47]
	v_pk_mul_f32 v[80:81], v[80:81], v[44:45]
	v_pk_mul_f32 v[108:109], v[108:109], v[32:33]
	v_pk_mul_f32 v[104:105], v[104:105], v[36:37]
	v_pk_mul_f32 v[100:101], v[100:101], v[40:41]
	v_pk_mul_f32 v[110:111], v[110:111], v[34:35]
	v_pk_mul_f32 v[106:107], v[106:107], v[38:39]
	v_pk_mul_f32 v[102:103], v[102:103], v[42:43]
	v_pk_mul_f32 v[98:99], v[98:99], v[46:47]
	v_pk_mul_f32 v[96:97], v[96:97], v[44:45]
	v_pk_mul_f32 v[124:125], v[124:125], v[32:33]
	v_pk_mul_f32 v[120:121], v[120:121], v[36:37]
	v_pk_mul_f32 v[116:117], v[116:117], v[40:41]
	v_pk_mul_f32 v[126:127], v[126:127], v[34:35]
	v_pk_mul_f32 v[122:123], v[122:123], v[38:39]
	v_pk_mul_f32 v[118:119], v[118:119], v[42:43]
	v_pk_mul_f32 v[114:115], v[114:115], v[46:47]
	v_pk_mul_f32 v[112:113], v[112:113], v[44:45]
	v_pk_mul_f32 v[140:141], v[140:141], v[32:33]
	v_pk_mul_f32 v[136:137], v[136:137], v[36:37]
	v_pk_mul_f32 v[132:133], v[132:133], v[40:41]
	v_pk_mul_f32 v[142:143], v[142:143], v[34:35]
	v_pk_mul_f32 v[138:139], v[138:139], v[38:39]
	v_pk_mul_f32 v[134:135], v[134:135], v[42:43]
	v_pk_mul_f32 v[130:131], v[130:131], v[46:47]
	v_pk_mul_f32 v[128:129], v[128:129], v[44:45]

; #define DS_LOAD(X, s) do { const int _s = (s) < NS - 1 ? (s) : NS - 1; const int _j = 64 * (c.a0 - 1 + _s) + sr; const unsigned _k0 = DS_KROW(_j) + (unsigned)sc, _k1 = DS_KROW(_j + 32) + (unsigned)sc; \
;         ks##X##0 = *(const u32x2*)(zb + _k0); vs##X##0 = *(const u32x2*)(zb + (_k0 + 1024u)); ks##X##1 = *(const u32x2*)(zb + _k1); vs##X##1 = *(const u32x2*)(zb + (_k1 + 1024u)); } while (0)
; #define DS_WRITE(X, b) do { *(LAS bf16x8*)(V_lds + (b) * SHM_T + vst0) = f8tob(vs##X##0); *(LAS bf16x8*)(K_lds + (b) * SHM_T + kst0) = f8tob(ks##X##0); \
;         *(LAS bf16x8*)(V_lds + (b) * SHM_T + vst1) = f8tob(vs##X##1); *(LAS bf16x8*)(K_lds + (b) * SHM_T + kst1) = f8tob(ks##X##1); } while (0)
; #define DS_LOADQ(pa) do { const unsigned _q = roff(64 * (c.a0 + (pa)) + 32 * par + r32) + (unsigned)hi * 8u; _Pragma("unroll") for (int d0 = 0; d0 < 8; ++d0) qraw[d0] = *(const u32x2*)(zb + (_q + d0 * 16u)); } while (0)
; #define DS_RESET() do { m_reg = -1e30f; l_reg = 0.f; _Pragma("unroll") for (int d = 0; d < 4; ++d) _Pragma("unroll") for (int r = 0; r < 16; ++r) o[d][r] = 0.f; } while (0)
; __device__ __forceinline__ void datt_stream(LAS unsigned char* lds, const DattRun& c, const float C, const int wv) {
;     ...
;     bf16x8 qr[8]; u32x2 qraw[8]; float m_reg = -1e30f, l_reg = 0.f; f32x16 o[4];
;     ...
;             if (act && rel <= 2) { compute(rel, q, pa); if (rel == 2 && pa + 4 < NP) DS_LOADQ(pa + 4); }
;             else if (act) { finish(pa); DS_RESET(); }
;             if (q == 0) { DS_WRITE(A, 1); DS_LOAD(A, st + 3); } else { DS_WRITE(B, 0); DS_LOAD(B, st + 3); }
.LBB0_523:
	s_waitcnt vmcnt(6)
	v_cvt_pk_f32_fp8_e32 v[66:67], v212
	v_cvt_pk_f32_fp8_sdwa v[68:69], v212 src0_sel:WORD_1
	v_cvt_pk_f32_fp8_e32 v[70:71], v213
	v_cvt_pk_f32_fp8_sdwa v[72:73], v213 src0_sel:WORD_1
	v_cvt_pk_bf16_f32 v66, v66, v67
	v_cvt_pk_bf16_f32 v67, v68, v69
	v_cvt_pk_bf16_f32 v68, v70, v71
	v_cvt_pk_bf16_f32 v69, v72, v73
	ds_write_b128 v225, v[66:69]
	v_cvt_pk_f32_fp8_e32 v[66:67], v210
	v_cvt_pk_f32_fp8_sdwa v[68:69], v210 src0_sel:WORD_1
	v_cvt_pk_f32_fp8_e32 v[70:71], v211
	v_cvt_pk_f32_fp8_sdwa v[72:73], v211 src0_sel:WORD_1
	v_cvt_pk_bf16_f32 v66, v66, v67
	v_cvt_pk_bf16_f32 v67, v68, v69
	v_cvt_pk_bf16_f32 v68, v70, v71
	v_cvt_pk_bf16_f32 v69, v72, v73
	s_add_i32 s6, s57, 4
	ds_write_b128 v226, v[66:69] offset:32768
	s_waitcnt vmcnt(5)
	v_cvt_pk_f32_fp8_e32 v[66:67], v204
	v_cvt_pk_f32_fp8_sdwa v[68:69], v204 src0_sel:WORD_1
	s_min_i32 s6, s6, s81
	v_cvt_pk_f32_fp8_e32 v[70:71], v205
	v_cvt_pk_f32_fp8_sdwa v[72:73], v205 src0_sel:WORD_1
	v_cvt_pk_bf16_f32 v66, v66, v67
	v_cvt_pk_bf16_f32 v67, v68, v69
	v_cvt_pk_bf16_f32 v68, v70, v71
	v_cvt_pk_bf16_f32 v69, v72, v73
	v_add_u32_e32 v64, s6, v224
	ds_write_b128 v227, v[66:69]
	s_waitcnt vmcnt(4)
	v_cvt_pk_f32_fp8_e32 v[66:67], v200
	v_cvt_pk_f32_fp8_sdwa v[68:69], v200 src0_sel:WORD_1
	v_cvt_pk_f32_fp8_e32 v[70:71], v201
	v_lshl_add_u32 v64, v64, 6, v197
	v_cvt_pk_bf16_f32 v66, v66, v67
	v_cvt_pk_bf16_f32 v67, v68, v69
	v_cvt_pk_bf16_f32 v68, v70, v71
	v_add_u32_e32 v70, 32, v64
	v_cvt_pk_f32_fp8_sdwa v[72:73], v201 src0_sel:WORD_1
	v_min_i32_e32 v70, s95, v70
	v_cmp_lt_i32_e32 vcc, s43, v64
	v_cvt_pk_bf16_f32 v69, v72, v73
	v_min_i32_e32 v72, s95, v64
	s_nop 0
	v_cndmask_b32_e32 v70, 0, v70, vcc
	v_cmp_lt_i32_e32 vcc, -1, v64
	v_lshlrev_b32_e32 v70, s45, v70
	v_add_u32_e32 v70, s56, v70
	v_cndmask_b32_e32 v64, 0, v72, vcc
	v_lshlrev_b32_e32 v64, s45, v64
	v_mad_u64_u32 v[70:71], s[6:7], v70, s42, v[196:197]
	v_add_u32_e32 v64, s56, v64
	v_add_u32_e32 v71, 0x400, v70
	v_mad_u64_u32 v[72:73], s[6:7], v64, s42, v[196:197]
	v_add_u32_e32 v64, 0x400, v72
	global_load_dwordx2 v[204:205], v71, s[92:93]
	global_load_dwordx2 v[212:213], v64, s[92:93]
	global_load_dwordx2 v[210:211], v72, s[92:93]
	global_load_dwordx2 v[200:201], v70, s[92:93]
	ds_write_b128 v228, v[66:69] offset:32768
	s_cmp_eq_u32 s101, 2
	s_cbranch_scc0 .Ldatt_qc1_skip
	v_cvt_pk_f32_fp8_e32 v[66:67], v176
	v_cvt_pk_f32_fp8_sdwa v[68:69], v176 src0_sel:WORD_1
	v_cvt_pk_f32_fp8_e32 v[70:71], v177
	v_cvt_pk_f32_fp8_sdwa v[72:73], v177 src0_sel:WORD_1
	v_cvt_pk_bf16_f32 v144, v66, v67
	v_cvt_pk_bf16_f32 v145, v68, v69
	v_cvt_pk_bf16_f32 v146, v70, v71
	v_cvt_pk_bf16_f32 v147, v72, v73
	v_cvt_pk_f32_fp8_e32 v[66:67], v178
	v_cvt_pk_f32_fp8_sdwa v[68:69], v178 src0_sel:WORD_1
	v_cvt_pk_f32_fp8_e32 v[70:71], v179
	v_cvt_pk_f32_fp8_sdwa v[72:73], v179 src0_sel:WORD_1
	v_cvt_pk_bf16_f32 v148, v66, v67
	v_cvt_pk_bf16_f32 v149, v68, v69
	v_cvt_pk_bf16_f32 v150, v70, v71
	v_cvt_pk_bf16_f32 v151, v72, v73
	v_cvt_pk_f32_fp8_e32 v[66:67], v180
	v_cvt_pk_f32_fp8_sdwa v[68:69], v180 src0_sel:WORD_1
	v_cvt_pk_f32_fp8_e32 v[70:71], v181
	v_cvt_pk_f32_fp8_sdwa v[72:73], v181 src0_sel:WORD_1
	v_cvt_pk_bf16_f32 v152, v66, v67
	v_cvt_pk_bf16_f32 v153, v68, v69
	v_cvt_pk_bf16_f32 v154, v70, v71
	v_cvt_pk_bf16_f32 v155, v72, v73
	v_cvt_pk_f32_fp8_e32 v[66:67], v182
	v_cvt_pk_f32_fp8_sdwa v[68:69], v182 src0_sel:WORD_1
	v_cvt_pk_f32_fp8_e32 v[70:71], v183
	v_cvt_pk_f32_fp8_sdwa v[72:73], v183 src0_sel:WORD_1
	v_cvt_pk_bf16_f32 v156, v66, v67
	v_cvt_pk_bf16_f32 v157, v68, v69
	v_cvt_pk_bf16_f32 v158, v70, v71
	v_cvt_pk_bf16_f32 v159, v72, v73
	v_cvt_pk_f32_fp8_e32 v[66:67], v184
	v_cvt_pk_f32_fp8_sdwa v[68:69], v184 src0_sel:WORD_1
	v_cvt_pk_f32_fp8_e32 v[70:71], v185
	v_cvt_pk_f32_fp8_sdwa v[72:73], v185 src0_sel:WORD_1
	v_cvt_pk_bf16_f32 v160, v66, v67
	v_cvt_pk_bf16_f32 v161, v68, v69
	v_cvt_pk_bf16_f32 v162, v70, v71
	v_cvt_pk_bf16_f32 v163, v72, v73
	v_cvt_pk_f32_fp8_e32 v[66:67], v188
	v_cvt_pk_f32_fp8_sdwa v[68:69], v188 src0_sel:WORD_1
	v_cvt_pk_f32_fp8_e32 v[70:71], v189
	v_cvt_pk_f32_fp8_sdwa v[72:73], v189 src0_sel:WORD_1
	v_cvt_pk_bf16_f32 v164, v66, v67
	v_cvt_pk_bf16_f32 v165, v68, v69
	v_cvt_pk_bf16_f32 v166, v70, v71
	v_cvt_pk_bf16_f32 v167, v72, v73
	v_cvt_pk_f32_fp8_e32 v[66:67], v190
	v_cvt_pk_f32_fp8_sdwa v[68:69], v190 src0_sel:WORD_1
	v_cvt_pk_f32_fp8_e32 v[70:71], v191
	v_cvt_pk_f32_fp8_sdwa v[72:73], v191 src0_sel:WORD_1
	v_cvt_pk_bf16_f32 v168, v66, v67
	v_cvt_pk_bf16_f32 v169, v68, v69
	v_cvt_pk_bf16_f32 v170, v70, v71
	v_cvt_pk_bf16_f32 v171, v72, v73
	v_cvt_pk_f32_fp8_e32 v[66:67], v192
	v_cvt_pk_f32_fp8_sdwa v[68:69], v192 src0_sel:WORD_1
	v_cvt_pk_f32_fp8_e32 v[70:71], v193
	v_cvt_pk_f32_fp8_sdwa v[72:73], v193 src0_sel:WORD_1
	v_cvt_pk_bf16_f32 v172, v66, v67
	v_cvt_pk_bf16_f32 v173, v68, v69
	v_cvt_pk_bf16_f32 v174, v70, v71
	v_cvt_pk_bf16_f32 v175, v72, v73
	s_mov_b32 s101, 3

; __device__ __forceinline__ int crow(int r, int hi) { return (r & 3) + 8 * (r >> 2) + 4 * hi; }
; template <int DK16, int DV32, bool MASK, int HALFWIN, bool RES, bool WT, class P>
; __device__ __forceinline__ void attn_unit(LAS unsigned char* lds, const P& c, const int ntiles, const float C, const int wv) {
;     ...
;             float pmax = -__builtin_inff();
;             if (do0) {
; #pragma unroll
;                 for (int r = 0; r < 16; ++r) pmax = fmaxf(pmax, p0[r]); }
;             if (do1) {
; #pragma unroll
;                 for (int r = 0; r < 16; ++r) pmax = fmaxf(pmax, p1[r]); }
;             { auto rr = __builtin_amdgcn_permlane32_swap(__float_as_uint(pmax), __float_as_uint(pmax), false, false);
;               pmax = fmaxf(__uint_as_float(rr[0]), __uint_as_float(rr[1])); }
;             const float mn = fmaxf(m_reg, pmax), alpha = __builtin_amdgcn_exp2f(m_reg - mn); m_reg = mn;
;             float ps = 0.f;
;             if (do0) {
; #pragma unroll
;                 for (int r = 0; r < 16; ++r) { p0[r] = __builtin_amdgcn_exp2f(p0[r] - mn); ps += p0[r]; } }
;             if (do1) {
; #pragma unroll
;                 for (int r = 0; r < 16; ++r) { p1[r] = __builtin_amdgcn_exp2f(p1[r] - mn); ps += p1[r]; } }
;             { auto rr = __builtin_amdgcn_permlane32_swap(__float_as_uint(ps), __float_as_uint(ps), false, false);
;               ps = __uint_as_float(rr[0]) + __uint_as_float(rr[1]); }
;             l_reg = l_reg * alpha + ps;
;             if (__any(alpha < 1.f)) { if (hi == 0) al_l[r32] = alpha; asm volatile("s_waitcnt lgkmcnt(0)" ::: "memory");
; #pragma unroll
;                 for (int r = 0; r < 16; ++r) { const float a = al_l[crow(r, hi)];
; #pragma unroll
;                     for (int d = 0; d < DV32; ++d) o[d][r] *= a; } }
.LBB0_660:
	v_max3_f32 v0, v122, s38, v123
	v_max3_f32 v0, v0, v78, v79
	v_max3_f32 v0, v0, v76, v77
	v_max3_f32 v0, v0, v74, v75
	v_max3_f32 v0, v0, v72, v73
	v_max3_f32 v0, v0, v70, v71
	v_max3_f32 v0, v0, v68, v69
	v_max3_f32 v0, v0, v66, v67
	v_max3_f32 v0, v0, v16, v17
	v_max3_f32 v0, v0, v18, v19
	v_max3_f32 v0, v0, v20, v21
	v_max3_f32 v0, v0, v22, v23
	v_max3_f32 v0, v0, v24, v25
	v_max3_f32 v0, v0, v26, v27
	v_max3_f32 v0, v0, v28, v29
	v_max3_f32 v0, v0, v30, v31
	v_mov_b32_e32 v1, v0
	s_nop 1
	v_permlane32_swap_b32_e32 v0, v1
	v_max3_f32 v157, v156, v0, v1
	v_sub_f32_e32 v1, v157, v156
	v_cmp_lt_f32_e32 vcc, 0x41000000, v1
	s_cbranch_vccnz .Llz_w0
	v_mov_b32_e32 v157, v156
.Llz_w0:
	v_sub_f32_e32 v0, v122, v157
	v_exp_f32_e32 v64, v0
	v_sub_f32_e32 v0, v123, v157
	v_exp_f32_e32 v122, v0
	v_sub_f32_e32 v0, v78, v157
	v_exp_f32_e32 v78, v0
	v_sub_f32_e32 v0, v79, v157
	v_exp_f32_e32 v79, v0
	v_sub_f32_e32 v1, v76, v157
	v_add_f32_e32 v0, 0, v64
	v_exp_f32_e32 v76, v1
	v_sub_f32_e32 v1, v77, v157
	v_add_f32_e32 v0, v122, v0
	v_exp_f32_e32 v77, v1
	v_sub_f32_e32 v1, v74, v157
	v_add_f32_e32 v0, v78, v0
	v_exp_f32_e32 v74, v1
	v_sub_f32_e32 v1, v75, v157
	v_add_f32_e32 v0, v79, v0
	v_exp_f32_e32 v75, v1
	v_sub_f32_e32 v1, v72, v157
	v_add_f32_e32 v0, v76, v0
	v_exp_f32_e32 v72, v1
	v_sub_f32_e32 v1, v73, v157
	v_add_f32_e32 v0, v77, v0
	v_exp_f32_e32 v73, v1
	v_sub_f32_e32 v1, v70, v157
	v_add_f32_e32 v0, v74, v0
	v_exp_f32_e32 v70, v1
	v_sub_f32_e32 v1, v71, v157
	v_add_f32_e32 v0, v75, v0
	v_exp_f32_e32 v71, v1
	v_sub_f32_e32 v1, v68, v157
	v_add_f32_e32 v0, v72, v0
	v_exp_f32_e32 v68, v1
	v_sub_f32_e32 v1, v69, v157
	v_add_f32_e32 v0, v73, v0
	v_exp_f32_e32 v69, v1
	v_sub_f32_e32 v1, v66, v157
	v_add_f32_e32 v0, v70, v0
	v_exp_f32_e32 v66, v1
	v_sub_f32_e32 v1, v67, v157
	v_add_f32_e32 v0, v71, v0
	v_exp_f32_e32 v67, v1
	v_add_f32_e32 v0, v68, v0
	v_add_f32_e32 v0, v69, v0
	v_add_f32_e32 v0, v66, v0
	v_add_f32_e32 v3, v67, v0
	v_sub_f32_e32 v0, v16, v157
	v_exp_f32_e32 v0, v0
	v_sub_f32_e32 v1, v17, v157
	v_exp_f32_e32 v1, v1
	v_sub_f32_e32 v2, v18, v157
	v_exp_f32_e32 v2, v2
	v_sub_f32_e32 v4, v19, v157
	v_exp_f32_e32 v4, v4
	v_sub_f32_e32 v5, v20, v157
	v_add_f32_e32 v3, v0, v3
	v_exp_f32_e32 v8, v5
	v_sub_f32_e32 v5, v21, v157
	v_add_f32_e32 v3, v1, v3
	v_exp_f32_e32 v12, v5
	v_sub_f32_e32 v5, v22, v157
	v_add_f32_e32 v3, v2, v3
	v_exp_f32_e32 v7, v5
	v_sub_f32_e32 v5, v23, v157
	v_add_f32_e32 v3, v4, v3
	v_exp_f32_e32 v11, v5
	v_add_f32_e32 v3, v8, v3
	v_add_f32_e32 v3, v12, v3
	v_add_f32_e32 v3, v7, v3
	v_add_f32_e32 v9, v11, v3
	v_sub_f32_e32 v3, v24, v157
	v_exp_f32_e32 v3, v3
	v_sub_f32_e32 v5, v25, v157
	v_exp_f32_e32 v5, v5
	v_sub_f32_e32 v6, v26, v157
	v_exp_f32_e32 v6, v6
	v_sub_f32_e32 v10, v27, v157
	v_exp_f32_e32 v10, v10
	v_add_f32_e32 v9, v3, v9
	v_add_f32_e32 v9, v5, v9
	v_add_f32_e32 v9, v6, v9
	v_add_f32_e32 v16, v10, v9
	v_sub_f32_e32 v9, v28, v157
	v_exp_f32_e32 v9, v9
	v_sub_f32_e32 v13, v29, v157
	v_exp_f32_e32 v13, v13
	v_sub_f32_e32 v14, v30, v157
	v_exp_f32_e32 v14, v14
	v_sub_f32_e32 v15, v31, v157
	v_exp_f32_e32 v15, v15
	v_add_f32_e32 v16, v9, v16
	v_add_f32_e32 v16, v13, v16
	v_sub_f32_e32 v124, v156, v157
	v_add_f32_e32 v16, v14, v16
	v_add_f32_e32 v17, v15, v16
	v_exp_f32_e32 v16, v124
	v_mov_b32_e32 v18, v17
	s_nop 1
	v_permlane32_swap_b32_e32 v17, v18
	v_cmp_gt_f32_e32 vcc, 1.0, v16
	s_cbranch_vccz .LBB0_664
	s_and_saveexec_b64 s[18:19], s[8:9]
	ds_write_b32 v146, v16 offset:128
	s_or_b64 exec, exec, s[18:19]
	s_waitcnt lgkmcnt(0)
	v_add_u32_e32 v19, s26, v116
	ds_read_b128 v[20:23], v19 offset:224
	ds_read_b128 v[24:27], v19 offset:192
	ds_read_b128 v[28:31], v19 offset:160
	ds_read_b128 v[124:127], v19 offset:128
	s_waitcnt lgkmcnt(3)
	v_pk_mul_f32 v[44:45], v[44:45], v[20:21]
	s_waitcnt lgkmcnt(2)
	v_pk_mul_f32 v[40:41], v[40:41], v[24:25]
	s_waitcnt lgkmcnt(1)
	v_pk_mul_f32 v[36:37], v[36:37], v[28:29]
	v_pk_mul_f32 v[46:47], v[46:47], v[22:23]
	v_pk_mul_f32 v[42:43], v[42:43], v[26:27]
	v_pk_mul_f32 v[38:39], v[38:39], v[30:31]
	s_waitcnt lgkmcnt(0)
	v_pk_mul_f32 v[34:35], v[34:35], v[126:127]
	v_pk_mul_f32 v[32:33], v[32:33], v[124:125]
	v_pk_mul_f32 v[60:61], v[60:61], v[20:21]
	v_pk_mul_f32 v[56:57], v[56:57], v[24:25]
	v_pk_mul_f32 v[52:53], v[52:53], v[28:29]
	v_pk_mul_f32 v[62:63], v[62:63], v[22:23]
	v_pk_mul_f32 v[58:59], v[58:59], v[26:27]
	v_pk_mul_f32 v[54:55], v[54:55], v[30:31]
	v_pk_mul_f32 v[50:51], v[50:51], v[126:127]
	v_pk_mul_f32 v[48:49], v[48:49], v[124:125]

; __device__ __forceinline__ int crow(int r, int hi) { return (r & 3) + 8 * (r >> 2) + 4 * hi; }
; template <int DK16, int DV32, bool MASK, int HALFWIN, bool RES, bool WT, class P>
; __device__ __forceinline__ void attn_unit(LAS unsigned char* lds, const P& c, const int ntiles, const float C, const int wv) {
;     ...
;             float pmax = -__builtin_inff();
;             if (do0) {
; #pragma unroll
;                 for (int r = 0; r < 16; ++r) pmax = fmaxf(pmax, p0[r]); }
;             if (do1) {
; #pragma unroll
;                 for (int r = 0; r < 16; ++r) pmax = fmaxf(pmax, p1[r]); }
;             { auto rr = __builtin_amdgcn_permlane32_swap(__float_as_uint(pmax), __float_as_uint(pmax), false, false);
;               pmax = fmaxf(__uint_as_float(rr[0]), __uint_as_float(rr[1])); }
;             const float mn = fmaxf(m_reg, pmax), alpha = __builtin_amdgcn_exp2f(m_reg - mn); m_reg = mn;
;             float ps = 0.f;
;             if (do0) {
; #pragma unroll
;                 for (int r = 0; r < 16; ++r) { p0[r] = __builtin_amdgcn_exp2f(p0[r] - mn); ps += p0[r]; } }
;             if (do1) {
; #pragma unroll
;                 for (int r = 0; r < 16; ++r) { p1[r] = __builtin_amdgcn_exp2f(p1[r] - mn); ps += p1[r]; } }
;             { auto rr = __builtin_amdgcn_permlane32_swap(__float_as_uint(ps), __float_as_uint(ps), false, false);
;               ps = __uint_as_float(rr[0]) + __uint_as_float(rr[1]); }
;             l_reg = l_reg * alpha + ps;
;             if (__any(alpha < 1.f)) { if (hi == 0) al_l[r32] = alpha; asm volatile("s_waitcnt lgkmcnt(0)" ::: "memory");
; #pragma unroll
;                 for (int r = 0; r < 16; ++r) { const float a = al_l[crow(r, hi)];
; #pragma unroll
;                     for (int d = 0; d < DV32; ++d) o[d][r] *= a; } }
.LBB0_673:
	v_max3_f32 v32, v122, s38, v123
	v_max3_f32 v32, v32, v78, v79
	v_max3_f32 v32, v32, v76, v77
	v_max3_f32 v32, v32, v74, v75
	v_max3_f32 v32, v32, v72, v73
	v_max3_f32 v32, v32, v70, v71
	v_max3_f32 v32, v32, v68, v69
	v_max3_f32 v32, v32, v66, v67
	v_max3_f32 v32, v32, v48, v49
	v_max3_f32 v32, v32, v50, v51
	v_max3_f32 v32, v32, v52, v53
	v_max3_f32 v32, v32, v54, v55
	v_max3_f32 v32, v32, v56, v57
	v_max3_f32 v32, v32, v58, v59
	v_max3_f32 v32, v32, v60, v61
	v_max3_f32 v32, v32, v62, v63
	v_mov_b32_e32 v33, v32
	s_nop 1
	v_permlane32_swap_b32_e32 v32, v33
	v_max3_f32 v156, v157, v32, v33
	v_sub_f32_e32 v33, v156, v157
	v_cmp_lt_f32_e32 vcc, 0x41000000, v33
	s_cbranch_vccnz .Llz_w1
	v_mov_b32_e32 v156, v157
.Llz_w1:
	v_sub_f32_e32 v33, v122, v156
	v_exp_f32_e32 v124, v33
	v_sub_f32_e32 v33, v123, v156
	v_exp_f32_e32 v123, v33
	v_sub_f32_e32 v33, v78, v156
	v_exp_f32_e32 v125, v33
	v_sub_f32_e32 v33, v79, v156
	v_exp_f32_e32 v126, v33
	v_sub_f32_e32 v34, v76, v156
	v_add_f32_e32 v33, 0, v124
	v_exp_f32_e32 v128, v34
	v_sub_f32_e32 v34, v77, v156
	v_add_f32_e32 v33, v123, v33
	v_exp_f32_e32 v131, v34
	v_sub_f32_e32 v34, v74, v156
	v_add_f32_e32 v33, v125, v33
	v_exp_f32_e32 v132, v34
	v_sub_f32_e32 v34, v75, v156
	v_add_f32_e32 v33, v126, v33
	v_exp_f32_e32 v134, v34
	v_sub_f32_e32 v34, v72, v156
	v_add_f32_e32 v33, v128, v33
	v_exp_f32_e32 v127, v34
	v_sub_f32_e32 v34, v73, v156
	v_add_f32_e32 v33, v131, v33
	v_exp_f32_e32 v129, v34
	v_sub_f32_e32 v34, v70, v156
	v_add_f32_e32 v33, v132, v33
	v_exp_f32_e32 v130, v34
	v_sub_f32_e32 v34, v71, v156
	v_add_f32_e32 v33, v134, v33
	v_exp_f32_e32 v133, v34
	v_sub_f32_e32 v34, v68, v156
	v_add_f32_e32 v33, v127, v33
	v_exp_f32_e32 v135, v34
	v_sub_f32_e32 v34, v69, v156
	v_add_f32_e32 v33, v129, v33
	v_exp_f32_e32 v136, v34
	v_sub_f32_e32 v34, v66, v156
	v_add_f32_e32 v33, v130, v33
	v_exp_f32_e32 v137, v34
	v_sub_f32_e32 v34, v67, v156
	v_add_f32_e32 v33, v133, v33
	v_exp_f32_e32 v138, v34
	v_sub_f32_e32 v34, v48, v156
	v_add_f32_e32 v33, v135, v33
	v_exp_f32_e32 v64, v34
	v_sub_f32_e32 v34, v49, v156
	v_add_f32_e32 v33, v136, v33
	v_exp_f32_e32 v66, v34
	v_sub_f32_e32 v34, v50, v156
	v_add_f32_e32 v33, v137, v33
	v_exp_f32_e32 v67, v34
	v_sub_f32_e32 v34, v51, v156
	v_add_f32_e32 v33, v138, v33
	v_exp_f32_e32 v69, v34
	v_sub_f32_e32 v34, v52, v156
	v_add_f32_e32 v33, v64, v33
	v_exp_f32_e32 v73, v34
	v_sub_f32_e32 v34, v53, v156
	v_add_f32_e32 v33, v66, v33
	v_exp_f32_e32 v77, v34
	v_sub_f32_e32 v34, v54, v156
	v_add_f32_e32 v33, v67, v33
	v_exp_f32_e32 v72, v34
	v_sub_f32_e32 v34, v55, v156
	v_add_f32_e32 v33, v69, v33
	v_exp_f32_e32 v76, v34
	v_sub_f32_e32 v34, v56, v156
	v_add_f32_e32 v33, v73, v33
	v_exp_f32_e32 v68, v34
	v_sub_f32_e32 v34, v57, v156
	v_add_f32_e32 v33, v77, v33
	v_exp_f32_e32 v70, v34
	v_sub_f32_e32 v34, v58, v156
	v_add_f32_e32 v33, v72, v33
	v_exp_f32_e32 v71, v34
	v_sub_f32_e32 v34, v59, v156
	v_add_f32_e32 v33, v76, v33
	v_exp_f32_e32 v75, v34
	v_sub_f32_e32 v34, v60, v156
	v_add_f32_e32 v33, v68, v33
	v_exp_f32_e32 v74, v34
	v_sub_f32_e32 v34, v61, v156
	v_add_f32_e32 v33, v70, v33
	v_exp_f32_e32 v78, v34
	v_sub_f32_e32 v34, v62, v156
	v_add_f32_e32 v33, v71, v33
	v_exp_f32_e32 v79, v34
	v_sub_f32_e32 v34, v63, v156
	v_add_f32_e32 v33, v75, v33
	v_exp_f32_e32 v122, v34
	v_sub_f32_e32 v32, v157, v156
	v_add_f32_e32 v33, v74, v33
	v_add_f32_e32 v33, v78, v33
	v_exp_f32_e32 v139, v32
	v_add_f32_e32 v33, v79, v33
	v_add_f32_e32 v154, v122, v33
	v_mov_b32_e32 v157, v154
	v_mov_b64_e32 v[46:47], v[30:31]
	v_mov_b64_e32 v[62:63], v[14:15]
	v_permlane32_swap_b32_e32 v154, v157
	v_cmp_gt_f32_e32 vcc, 1.0, v139
	v_mov_b64_e32 v[44:45], v[28:29]
	v_mov_b64_e32 v[42:43], v[26:27]
	v_mov_b64_e32 v[40:41], v[24:25]
	v_mov_b64_e32 v[38:39], v[22:23]
	v_mov_b64_e32 v[36:37], v[20:21]
	v_mov_b64_e32 v[34:35], v[18:19]
	v_mov_b64_e32 v[32:33], v[16:17]
	v_mov_b64_e32 v[60:61], v[12:13]
	v_mov_b64_e32 v[58:59], v[10:11]
	v_mov_b64_e32 v[56:57], v[8:9]
	v_mov_b64_e32 v[54:55], v[6:7]
	v_mov_b64_e32 v[52:53], v[4:5]
	v_mov_b64_e32 v[50:51], v[2:3]
	v_mov_b64_e32 v[48:49], v[0:1]
	s_cbranch_vccz .LBB0_677
	s_and_saveexec_b64 s[10:11], s[8:9]
	ds_write_b32 v146, v139 offset:128
	s_or_b64 exec, exec, s[10:11]
	s_waitcnt lgkmcnt(0)
	v_add_u32_e32 v32, s26, v116
	ds_read_b128 v[48:51], v32 offset:224
	ds_read_b128 v[52:55], v32 offset:192
	ds_read_b128 v[158:161], v32 offset:160
	ds_read_b128 v[162:165], v32 offset:128
	s_waitcnt lgkmcnt(3)
	v_pk_mul_f32 v[44:45], v[28:29], v[48:49]
	s_waitcnt lgkmcnt(2)
	v_pk_mul_f32 v[40:41], v[24:25], v[52:53]
	s_waitcnt lgkmcnt(1)
	v_pk_mul_f32 v[36:37], v[20:21], v[158:159]
	v_pk_mul_f32 v[46:47], v[30:31], v[50:51]
	v_pk_mul_f32 v[42:43], v[26:27], v[54:55]
	v_pk_mul_f32 v[38:39], v[22:23], v[160:161]
	s_waitcnt lgkmcnt(0)
	v_pk_mul_f32 v[34:35], v[18:19], v[164:165]
	v_pk_mul_f32 v[32:33], v[16:17], v[162:163]
	v_pk_mul_f32 v[60:61], v[12:13], v[48:49]
	v_pk_mul_f32 v[56:57], v[8:9], v[52:53]
	v_pk_mul_f32 v[52:53], v[4:5], v[158:159]
	v_pk_mul_f32 v[62:63], v[14:15], v[50:51]
	v_pk_mul_f32 v[58:59], v[10:11], v[54:55]
	v_pk_mul_f32 v[54:55], v[6:7], v[160:161]
	v_pk_mul_f32 v[50:51], v[2:3], v[164:165]
	v_pk_mul_f32 v[48:49], v[0:1], v[162:163]

; #define LAS __attribute__((address_space(3)))
; template <int DA, int DB, int H> __device__ __forceinline__ void pv_half2(f32x16& oa, f32x16& ob, int vb, bf16x8 paA, bf16x8 paB) {
;     const s16x4 l0 = tr_read<v_rd_off(DA, 2 * H, 0)>(vb), h0 = tr_read<v_rd_off(DA, 2 * H, 1)>(vb), l1 = tr_read<v_rd_off(DA, 2 * H + 1, 0)>(vb), h1 = tr_read<v_rd_off(DA, 2 * H + 1, 1)>(vb);
;     const s16x4 m0 = tr_read<v_rd_off(DB, 2 * H, 0)>(vb), g0 = tr_read<v_rd_off(DB, 2 * H, 1)>(vb), m1 = tr_read<v_rd_off(DB, 2 * H + 1, 0)>(vb), g1 = tr_read<v_rd_off(DB, 2 * H + 1, 1)>(vb);
;     asm volatile("s_waitcnt lgkmcnt(0)" ::: "memory"); __builtin_amdgcn_sched_barrier(0);
;     ...
;     oa = __builtin_amdgcn_mfma_f32_32x32x16_bf16(paA, ATT_PK(l0, h0), oa, 0, 0, 0);
;     ob = __builtin_amdgcn_mfma_f32_32x32x16_bf16(paA, ATT_PK(m0, g0), ob, 0, 0, 0);
;     oa = __builtin_amdgcn_mfma_f32_32x32x16_bf16(paB, ATT_PK(l1, h1), oa, 0, 0, 0);
;     ob = __builtin_amdgcn_mfma_f32_32x32x16_bf16(paB, ATT_PK(m1, g1), ob, 0, 0, 0);
;     ...
; }
; template <int DK16, int DV32, bool MASK, int HALFWIN, bool RES, bool WT, class P>
; __device__ __forceinline__ void attn_unit(LAS unsigned char* lds, const P& c, const int ntiles, const float C, const int wv) {
;     ...
;             const LAS unsigned char* Ks = K_lds + b * SHM_T;
;             if (do0) {
; #pragma unroll
;                 for (int d0 = 0; d0 < DK16; ++d0) { const bf16x8 b0 = *(const LAS bf16x8*)(Ks + ATT_KSWZ(r32, (d0 * 16 + hi * 8) * 2)); p0 = __builtin_amdgcn_mfma_f32_32x32x16_bf16(b0, qr[d0], p0, 0, 0, 0); } }
;             if (do1) {
; #pragma unroll
;                 for (int d0 = 0; d0 < DK16; ++d0) { const bf16x8 b1 = *(const LAS bf16x8*)(Ks + ATT_KSWZ(32 + r32, (d0 * 16 + hi * 8) * 2)); p1 = __builtin_amdgcn_mfma_f32_32x32x16_bf16(b1, qr[d0], p1, 0, 0, 0); } }
.LBB0_1202:
	v_lshlrev_b32_e32 v33, 4, v155
	v_lshlrev_b32_e32 v32, 3, v155
	v_and_b32_e32 v33, 0xc0, v33
	v_lshlrev_b32_e32 v160, 1, v155
	v_and_or_b32 v33, v32, 24, v33
	v_and_b32_e32 v34, 32, v160
	v_and_b32_e32 v32, 0x100, v32
	v_or3_b32 v170, v33, v34, v32
	v_add_u32_e32 v96, 0x100, v170
	v_cvt_pk_bf16_f32 v76, v16, v17
	v_cvt_pk_bf16_f32 v77, v18, v19
	v_cvt_pk_bf16_f32 v78, v20, v21
	v_cvt_pk_bf16_f32 v79, v22, v23
	v_cvt_pk_bf16_f32 v80, v24, v25
	v_cvt_pk_bf16_f32 v81, v26, v27
	v_cvt_pk_bf16_f32 v82, v28, v29
	v_cvt_pk_bf16_f32 v83, v30, v31
	ds_read_b64_tr_b16 v[32:33], v96 offset:0
	ds_read_b64_tr_b16 v[34:35], v96 offset:0x800
	ds_read_b64_tr_b16 v[54:55], v96 offset:0x1000
	ds_read_b64_tr_b16 v[56:57], v96 offset:0x1800
	ds_read_b64_tr_b16 v[58:59], v96 offset:0x200
	ds_read_b64_tr_b16 v[60:61], v96 offset:0xa00
	ds_read_b64_tr_b16 v[84:85], v96 offset:0x1200
	ds_read_b64_tr_b16 v[86:87], v96 offset:0x1a00
	s_waitcnt lgkmcnt(0)
	s_nop 0
	v_permlane32_swap_b32_e32 v76, v78
	v_permlane32_swap_b32_e32 v77, v79
	v_permlane32_swap_b32_e32 v80, v82
	v_permlane32_swap_b32_e32 v81, v83
	v_mfma_f32_32x32x16_bf16 v[16:31], v[76:79], v[32:35], v[0:15]
	v_mfma_f32_32x32x16_bf16 v[32:47], v[76:79], v[58:61], v[0:15]
	v_mfma_f32_32x32x16_bf16 v[32:47], v[80:83], v[84:87], v[32:47]
	ds_read_b64_tr_b16 v[84:85], v96 offset:0x400
	ds_read_b64_tr_b16 v[86:87], v96 offset:0xc00
	ds_read_b64_tr_b16 v[88:89], v96 offset:0x1400
	ds_read_b64_tr_b16 v[90:91], v96 offset:0x1c00
	ds_read_b64_tr_b16 v[92:93], v96 offset:0x600
	ds_read_b64_tr_b16 v[94:95], v96 offset:0xe00
	ds_read_b64_tr_b16 v[138:139], v96 offset:0x1600
	v_mfma_f32_32x32x16_bf16 v[16:31], v[80:83], v[54:57], v[16:31]
	ds_read_b64_tr_b16 v[140:141], v96 offset:0x1e00
	s_waitcnt lgkmcnt(0)
	v_cvt_pk_bf16_f32 v134, v48, v49
	v_cvt_pk_bf16_f32 v135, v50, v51
	v_cvt_pk_bf16_f32 v136, v52, v53
	v_mfma_f32_32x32x16_bf16 v[48:63], v[76:79], v[84:87], v[0:15]
	v_cvt_pk_bf16_f32 v137, v66, v67
	v_cvt_pk_bf16_f32 v130, v68, v69
	v_cvt_pk_bf16_f32 v131, v70, v71
	v_cvt_pk_bf16_f32 v132, v72, v73
	v_cvt_pk_bf16_f32 v133, v74, v75
	ds_read_b64_tr_b16 v[66:67], v96 offset:0x2000
	ds_read_b64_tr_b16 v[68:69], v96 offset:0x2800
	v_mfma_f32_32x32x16_bf16 v[0:15], v[76:79], v[92:95], v[0:15]
	ds_read_b64_tr_b16 v[70:71], v96 offset:0x3000
	ds_read_b64_tr_b16 v[72:73], v96 offset:0x3800
	ds_read_b64_tr_b16 v[74:75], v96 offset:0x2200
	ds_read_b64_tr_b16 v[76:77], v96 offset:0x2a00
	ds_read_b64_tr_b16 v[84:85], v96 offset:0x3200
	ds_read_b64_tr_b16 v[86:87], v96 offset:0x3a00
	s_waitcnt lgkmcnt(0)
	v_mfma_f32_32x32x16_bf16 v[48:63], v[80:83], v[88:91], v[48:63]
	v_permlane32_swap_b32_e32 v134, v136
	v_permlane32_swap_b32_e32 v135, v137
	v_permlane32_swap_b32_e32 v130, v132
	v_permlane32_swap_b32_e32 v131, v133
	v_mfma_f32_32x32x16_bf16 v[0:15], v[80:83], v[138:141], v[0:15]
	v_mfma_f32_32x32x16_bf16 v[16:31], v[134:137], v[66:69], v[16:31]
	ds_read_b64_tr_b16 v[150:151], v96 offset:0x2400
	ds_read_b64_tr_b16 v[152:153], v96 offset:0x2c00
	ds_read_b64_tr_b16 v[142:143], v96 offset:0x3400
	ds_read_b64_tr_b16 v[144:145], v96 offset:0x3c00
	ds_read_b64_tr_b16 v[146:147], v96 offset:0x2600
	ds_read_b64_tr_b16 v[148:149], v96 offset:0x2e00
	ds_read_b64_tr_b16 v[138:139], v96 offset:0x3600
	v_mfma_f32_32x32x16_bf16 v[32:47], v[134:137], v[74:77], v[32:47]
	ds_read_b64_tr_b16 v[140:141], v96 offset:0x3e00
	s_waitcnt lgkmcnt(0)
	v_mfma_f32_32x32x16_bf16 v[16:31], v[130:133], v[70:73], v[16:31]
	v_mfma_f32_32x32x16_bf16 v[32:47], v[130:133], v[84:87], v[32:47]
	v_add_u32_e32 v176, s47, v168
	v_add_u32_e32 v86, v176, v169
	ds_read_b128 v[66:69], v86 offset:8192
	v_add_u32_e32 v172, v176, v162
	ds_read_b128 v[82:85], v172 offset:8192
	v_add_u32_e32 v177, v176, v163
	v_add_u32_e32 v178, v176, v164
	v_add_u32_e32 v179, v176, v165
	v_add_u32_e32 v180, v176, v166
	v_add_u32_e32 v181, v176, v167
	v_add_u32_e32 v176, v176, v161
	s_waitcnt lgkmcnt(1)
	v_mfma_f32_32x32x16_bf16 v[66:81], v[66:69], v[126:129], 0
	ds_read_b128 v[172:175], v172
	s_waitcnt lgkmcnt(1)
	v_mfma_f32_32x32x16_bf16 v[66:81], v[82:85], v[122:125], v[66:81]
	ds_read_b128 v[82:85], v177 offset:8192
	s_waitcnt lgkmcnt(0)
	v_mfma_f32_32x32x16_bf16 v[66:81], v[82:85], v[118:121], v[66:81]
	ds_read_b128 v[82:85], v178 offset:8192
	s_waitcnt lgkmcnt(0)
	v_mfma_f32_32x32x16_bf16 v[66:81], v[82:85], v[114:117], v[66:81]
	ds_read_b128 v[82:85], v179 offset:8192
	s_waitcnt lgkmcnt(0)
	v_mfma_f32_32x32x16_bf16 v[66:81], v[82:85], v[110:113], v[66:81]
	ds_read_b128 v[82:85], v180 offset:8192
	s_waitcnt lgkmcnt(0)
	v_mfma_f32_32x32x16_bf16 v[66:81], v[82:85], v[106:109], v[66:81]
	ds_read_b128 v[82:85], v181 offset:8192
	s_waitcnt lgkmcnt(0)
	v_mfma_f32_32x32x16_bf16 v[66:81], v[82:85], v[102:105], v[66:81]
	ds_read_b128 v[82:85], v86
	s_waitcnt lgkmcnt(0)
	v_mfma_f32_32x32x16_bf16 v[82:97], v[82:85], v[126:129], 0
	v_mfma_f32_32x32x16_bf16 v[82:97], v[172:175], v[122:125], v[82:97]
	ds_read_b128 v[172:175], v177
	s_waitcnt lgkmcnt(0)
	v_mfma_f32_32x32x16_bf16 v[82:97], v[172:175], v[118:121], v[82:97]
	ds_read_b128 v[172:175], v178
	s_waitcnt lgkmcnt(0)
	v_mfma_f32_32x32x16_bf16 v[82:97], v[172:175], v[114:117], v[82:97]
	ds_read_b128 v[172:175], v179
	s_waitcnt lgkmcnt(0)
	v_mfma_f32_32x32x16_bf16 v[82:97], v[172:175], v[110:113], v[82:97]
	ds_read_b128 v[172:175], v180
	s_waitcnt lgkmcnt(0)
	v_mfma_f32_32x32x16_bf16 v[82:97], v[172:175], v[106:109], v[82:97]
	ds_read_b128 v[172:175], v181
	s_waitcnt lgkmcnt(0)
	v_mfma_f32_32x32x16_bf16 v[82:97], v[172:175], v[102:105], v[82:97]
	ds_read_b128 v[172:175], v176
	s_waitcnt lgkmcnt(0)
; __device__ __forceinline__ int crow(int r, int hi) { return (r & 3) + 8 * (r >> 2) + 4 * hi; }
; template <int DK16, int DV32, bool MASK, int HALFWIN, bool RES, bool WT, class P>
; __device__ __forceinline__ void attn_unit(LAS unsigned char* lds, const P& c, const int ntiles, const float C, const int wv) {
;     ...
;             } else {
; #pragma unroll
;                 for (int r = 0; r < 16; ++r) { p0[r] *= C; p1[r] *= C; }
;             }
;             float pmax = -__builtin_inff();
;             if (do0) {
; #pragma unroll
;                 for (int r = 0; r < 16; ++r) pmax = fmaxf(pmax, p0[r]); }
;             if (do1) {
; #pragma unroll
;                 for (int r = 0; r < 16; ++r) pmax = fmaxf(pmax, p1[r]); }
;             { auto rr = __builtin_amdgcn_permlane32_swap(__float_as_uint(pmax), __float_as_uint(pmax), false, false);
;               pmax = fmaxf(__uint_as_float(rr[0]), __uint_as_float(rr[1])); }
;             const float mn = fmaxf(m_reg, pmax), alpha = __builtin_amdgcn_exp2f(m_reg - mn); m_reg = mn;
;             float ps = 0.f;
;             if (do0) {
; #pragma unroll
;                 for (int r = 0; r < 16; ++r) { p0[r] = __builtin_amdgcn_exp2f(p0[r] - mn); ps += p0[r]; } }
;             if (do1) {
; #pragma unroll
;                 for (int r = 0; r < 16; ++r) { p1[r] = __builtin_amdgcn_exp2f(p1[r] - mn); ps += p1[r]; } }
;             { auto rr = __builtin_amdgcn_permlane32_swap(__float_as_uint(ps), __float_as_uint(ps), false, false);
;               ps = __uint_as_float(rr[0]) + __uint_as_float(rr[1]); }
;             l_reg = l_reg * alpha + ps;
;             if (__any(alpha < 1.f)) { if (hi == 0) al_l[r32] = alpha; asm volatile("s_waitcnt lgkmcnt(0)" ::: "memory");
; #pragma unroll
;                 for (int r = 0; r < 16; ++r) { const float a = al_l[crow(r, hi)];
; #pragma unroll
;                     for (int d = 0; d < DV32; ++d) o[d][r] *= a; } }
	v_mfma_f32_32x32x16_bf16 v[82:97], v[172:175], v[98:101], v[82:97]
	ds_read_b128 v[172:175], v176 offset:8192
	s_waitcnt lgkmcnt(0)
	v_mfma_f32_32x32x16_bf16 v[66:81], v[172:175], v[98:101], v[66:81]
	s_nop 8
	v_mul_f32_e32 v176, 0x3e0293ee, v82
	v_mul_f32_e32 v173, 0x3e0293ee, v83
	v_mul_f32_e32 v175, 0x3e0293ee, v84
	v_mul_f32_e32 v178, 0x3e0293ee, v85
	v_max3_f32 v173, v176, s38, v173
	v_mul_f32_e32 v180, 0x3e0293ee, v86
	v_mul_f32_e32 v182, 0x3e0293ee, v87
	v_max3_f32 v173, v173, v175, v178
	v_mul_f32_e32 v184, 0x3e0293ee, v88
	v_mul_f32_e32 v186, 0x3e0293ee, v89
	v_max3_f32 v173, v173, v180, v182
	v_mul_f32_e32 v188, 0x3e0293ee, v90
	v_mul_f32_e32 v190, 0x3e0293ee, v91
	v_max3_f32 v173, v173, v184, v186
	v_mul_f32_e32 v192, 0x3e0293ee, v92
	v_mul_f32_e32 v194, 0x3e0293ee, v93
	v_max3_f32 v173, v173, v188, v190
	v_mul_f32_e32 v196, 0x3e0293ee, v94
	v_mul_f32_e32 v198, 0x3e0293ee, v95
	v_max3_f32 v173, v173, v192, v194
	v_mul_f32_e32 v200, 0x3e0293ee, v96
	v_mul_f32_e32 v202, 0x3e0293ee, v97
	v_max3_f32 v173, v173, v196, v198
	v_mul_f32_e32 v172, 0x3e0293ee, v66
	v_mul_f32_e32 v174, 0x3e0293ee, v67
	v_max3_f32 v173, v173, v200, v202
	v_mul_f32_e32 v177, 0x3e0293ee, v68
	v_mul_f32_e32 v179, 0x3e0293ee, v69
	v_max3_f32 v172, v173, v172, v174
	v_mul_f32_e32 v181, 0x3e0293ee, v70
	v_mul_f32_e32 v183, 0x3e0293ee, v71
	v_max3_f32 v172, v172, v177, v179
	v_mul_f32_e32 v185, 0x3e0293ee, v72
	v_mul_f32_e32 v187, 0x3e0293ee, v73
	v_max3_f32 v172, v172, v181, v183
	v_mul_f32_e32 v189, 0x3e0293ee, v74
	v_mul_f32_e32 v191, 0x3e0293ee, v75
	v_max3_f32 v172, v172, v185, v187
	v_mul_f32_e32 v193, 0x3e0293ee, v76
	v_mul_f32_e32 v195, 0x3e0293ee, v77
	v_max3_f32 v172, v172, v189, v191
	v_mul_f32_e32 v197, 0x3e0293ee, v78
	v_mul_f32_e32 v199, 0x3e0293ee, v79
	v_max3_f32 v172, v172, v193, v195
	v_mul_f32_e32 v201, 0x3e0293ee, v80
	v_mul_f32_e32 v203, 0x3e0293ee, v81
	v_max3_f32 v172, v172, v197, v199
	v_max3_f32 v172, v172, v201, v203
	v_mov_b32_e32 v173, v172
	s_nop 1
	v_permlane32_swap_b32_e32 v172, v173
	v_max3_f32 v174, v171, v172, v173
	v_sub_f32_e32 v173, v174, v171
	v_cmp_lt_f32_e32 vcc, 0x41000000, v173
	s_cbranch_vccnz .Llz_x1
	v_mov_b32_e32 v174, v171
.Llz_x1:
	v_fma_f32 v82, v82, s94, -v174
	v_exp_f32_e32 v175, v82
	v_fma_f32 v83, v83, s94, -v174
	v_exp_f32_e32 v83, v83
	v_fma_f32 v84, v84, s94, -v174
	v_exp_f32_e32 v84, v84
	v_fma_f32 v85, v85, s94, -v174
	v_exp_f32_e32 v85, v85
	v_fma_f32 v86, v86, s94, -v174
	v_add_f32_e32 v82, 0, v175
	v_exp_f32_e32 v86, v86
	v_fma_f32 v87, v87, s94, -v174
	v_add_f32_e32 v82, v83, v82
	v_exp_f32_e32 v176, v87
	v_fma_f32 v87, v88, s94, -v174
	v_add_f32_e32 v82, v84, v82
	v_exp_f32_e32 v88, v87
	v_fma_f32 v87, v89, s94, -v174
	v_add_f32_e32 v82, v85, v82
	v_exp_f32_e32 v89, v87
	v_fma_f32 v87, v90, s94, -v174
	v_add_f32_e32 v82, v86, v82
	v_exp_f32_e32 v87, v87
	v_fma_f32 v90, v91, s94, -v174
	v_add_f32_e32 v82, v176, v82
	v_exp_f32_e32 v90, v90
	v_fma_f32 v91, v92, s94, -v174
	v_add_f32_e32 v82, v88, v82
	v_exp_f32_e32 v91, v91
	v_fma_f32 v92, v93, s94, -v174
	v_add_f32_e32 v82, v89, v82
	v_exp_f32_e32 v92, v92
	v_fma_f32 v93, v94, s94, -v174
	v_add_f32_e32 v82, v87, v82
	v_exp_f32_e32 v93, v93
	v_fma_f32 v94, v95, s94, -v174
	v_add_f32_e32 v82, v90, v82
	v_exp_f32_e32 v94, v94
	v_fma_f32 v95, v96, s94, -v174
	v_add_f32_e32 v82, v91, v82
	v_exp_f32_e32 v95, v95
	v_fma_f32 v96, v97, s94, -v174
	v_add_f32_e32 v82, v92, v82
	v_exp_f32_e32 v96, v96
	v_fma_f32 v66, v66, s94, -v174
	v_add_f32_e32 v82, v93, v82
	v_exp_f32_e32 v66, v66
	v_fma_f32 v67, v67, s94, -v174
	v_add_f32_e32 v82, v94, v82
	v_exp_f32_e32 v67, v67
	v_fma_f32 v68, v68, s94, -v174
	v_add_f32_e32 v82, v95, v82
	v_exp_f32_e32 v68, v68
	v_fma_f32 v69, v69, s94, -v174
	v_add_f32_e32 v82, v96, v82
	v_exp_f32_e32 v69, v69
	v_add_f32_e32 v82, v66, v82
	v_add_f32_e32 v82, v67, v82
	v_fma_f32 v70, v70, s94, -v174
	v_add_f32_e32 v82, v68, v82
	v_exp_f32_e32 v70, v70
	v_fma_f32 v71, v71, s94, -v174
	v_add_f32_e32 v97, v69, v82
	v_exp_f32_e32 v82, v71
	v_fma_f32 v71, v72, s94, -v174
	v_exp_f32_e32 v71, v71
	v_fma_f32 v72, v73, s94, -v174
	v_exp_f32_e32 v73, v72
	v_add_f32_e32 v72, v70, v97
	v_add_f32_e32 v72, v82, v72
	v_add_f32_e32 v72, v71, v72
	v_add_f32_e32 v97, v73, v72
	v_fma_f32 v72, v74, s94, -v174
	v_exp_f32_e32 v72, v72
	v_fma_f32 v74, v75, s94, -v174
	v_exp_f32_e32 v74, v74
	v_fma_f32 v75, v76, s94, -v174
	v_mfma_f32_32x32x16_bf16 v[48:63], v[134:137], v[150:153], v[48:63]
	v_exp_f32_e32 v75, v75
	v_fma_f32 v76, v77, s94, -v174
	v_exp_f32_e32 v76, v76
	v_add_f32_e32 v77, v72, v97
	v_add_f32_e32 v77, v74, v77
	v_add_f32_e32 v77, v75, v77
	v_add_f32_e32 v97, v76, v77
	v_mfma_f32_32x32x16_bf16 v[0:15], v[134:137], v[146:149], v[0:15]
	v_fma_f32 v77, v78, s94, -v174
	v_exp_f32_e32 v77, v77
	v_fma_f32 v78, v79, s94, -v174
	v_exp_f32_e32 v78, v78
	v_fma_f32 v79, v80, s94, -v174
	v_exp_f32_e32 v79, v79
	v_fma_f32 v80, v81, s94, -v174
	v_mfma_f32_32x32x16_bf16 v[48:63], v[130:133], v[142:145], v[48:63]
	v_exp_f32_e32 v80, v80
	v_sub_f32_e32 v171, v171, v174
	v_add_f32_e32 v81, v77, v97
	v_add_f32_e32 v81, v78, v81
	v_exp_f32_e32 v171, v171
	v_add_f32_e32 v81, v79, v81
	v_add_f32_e32 v172, v80, v81
	v_mfma_f32_32x32x16_bf16 v[0:15], v[130:133], v[138:141], v[0:15]
	v_mov_b32_e32 v173, v172
	s_nop 1
	v_permlane32_swap_b32_e32 v172, v173
	v_cmp_gt_f32_e32 vcc, 1.0, v171
	s_cbranch_vccz .LBB0_1206
; __device__ __forceinline__ int crow(int r, int hi) { return (r & 3) + 8 * (r >> 2) + 4 * hi; }
; template <int DK16, int DV32, bool MASK, int HALFWIN, bool RES, bool WT, class P>
; __device__ __forceinline__ void attn_unit(LAS unsigned char* lds, const P& c, const int ntiles, const float C, const int wv) {
;     ...
;             if (__any(alpha < 1.f)) { if (hi == 0) al_l[r32] = alpha; asm volatile("s_waitcnt lgkmcnt(0)" ::: "memory");
; #pragma unroll
;                 for (int r = 0; r < 16; ++r) { const float a = al_l[crow(r, hi)];
; #pragma unroll
;                     for (int d = 0; d < DV32; ++d) o[d][r] *= a; } }
;             const int vb = vb0 + b * SHM_T;
;     ...
;             if (do0) { bf16x8 pa0, pa1; ATT_PK4(p0, 0, pa0); ATT_PK4(p0, 8, pa1);
;                 pv_half2<0, 1, 0>(o[0], o[1], vb, pa0, pa1);
;                 if constexpr (DV32 == 4) { pv_half2<2, 3, 0>(o[2], o[3], vb, pa0, pa1); } }
;             if (do1) { bf16x8 pa2, pa3; ATT_PK4(p1, 0, pa2); ATT_PK4(p1, 8, pa3);
;                 pv_half2<0, 1, 1>(o[0], o[1], vb, pa2, pa3);
;                 if constexpr (DV32 == 4) { pv_half2<2, 3, 1>(o[2], o[3], vb, pa2, pa3); } }
	v_cmp_gt_u32_e32 vcc, 32, v155
	s_and_saveexec_b64 s[0:1], vcc
	v_lshl_add_u32 v81, v156, 2, s10
	ds_write_b32 v81, v171 offset:128
	s_or_b64 exec, exec, s[0:1]
	s_waitcnt lgkmcnt(0)
	v_add_u32_e32 v81, s10, v64
	ds_read_b128 v[130:133], v81 offset:224
	ds_read_b128 v[134:137], v81 offset:192
	ds_read_b128 v[138:141], v81 offset:160
	ds_read_b128 v[142:145], v81 offset:128
	s_waitcnt lgkmcnt(3)
	v_pk_mul_f32 v[28:29], v[28:29], v[130:131]
	s_waitcnt lgkmcnt(2)
	v_pk_mul_f32 v[24:25], v[24:25], v[134:135]
	s_waitcnt lgkmcnt(1)
	v_pk_mul_f32 v[20:21], v[20:21], v[138:139]
	v_pk_mul_f32 v[30:31], v[30:31], v[132:133]
	v_pk_mul_f32 v[26:27], v[26:27], v[136:137]
	v_pk_mul_f32 v[22:23], v[22:23], v[140:141]
	s_waitcnt lgkmcnt(0)
	v_pk_mul_f32 v[18:19], v[18:19], v[144:145]
	v_pk_mul_f32 v[16:17], v[16:17], v[142:143]
	v_pk_mul_f32 v[44:45], v[44:45], v[130:131]
	v_pk_mul_f32 v[40:41], v[40:41], v[134:135]
	v_pk_mul_f32 v[36:37], v[36:37], v[138:139]
	v_pk_mul_f32 v[46:47], v[46:47], v[132:133]
	v_pk_mul_f32 v[42:43], v[42:43], v[136:137]
	v_pk_mul_f32 v[38:39], v[38:39], v[140:141]
	v_pk_mul_f32 v[34:35], v[34:35], v[144:145]
	v_pk_mul_f32 v[32:33], v[32:33], v[142:143]
	v_pk_mul_f32 v[60:61], v[60:61], v[130:131]
	v_pk_mul_f32 v[56:57], v[56:57], v[134:135]
	v_pk_mul_f32 v[52:53], v[52:53], v[138:139]
	v_pk_mul_f32 v[62:63], v[62:63], v[132:133]
	v_pk_mul_f32 v[58:59], v[58:59], v[136:137]
	v_pk_mul_f32 v[54:55], v[54:55], v[140:141]
	v_pk_mul_f32 v[50:51], v[50:51], v[144:145]
	v_pk_mul_f32 v[48:49], v[48:49], v[142:143]
	v_pk_mul_f32 v[12:13], v[12:13], v[130:131]
	v_pk_mul_f32 v[8:9], v[8:9], v[134:135]
	v_pk_mul_f32 v[4:5], v[4:5], v[138:139]
	v_pk_mul_f32 v[14:15], v[14:15], v[132:133]
	v_pk_mul_f32 v[10:11], v[10:11], v[136:137]
	v_pk_mul_f32 v[6:7], v[6:7], v[140:141]
	v_pk_mul_f32 v[2:3], v[2:3], v[144:145]
	v_pk_mul_f32 v[0:1], v[0:1], v[142:143]
.LBB0_1206:
	s_add_i32 s0, s59, 0x100
	v_add_u32_e32 v97, s0, v170
	v_cvt_pk_bf16_f32 v130, v175, v83
	v_cvt_pk_bf16_f32 v131, v84, v85
	v_cvt_pk_bf16_f32 v132, v86, v176
	v_cvt_pk_bf16_f32 v133, v88, v89
	v_cvt_pk_bf16_f32 v84, v87, v90
	v_cvt_pk_bf16_f32 v85, v91, v92
	v_cvt_pk_bf16_f32 v86, v93, v94
	v_cvt_pk_bf16_f32 v87, v95, v96
	ds_read_b64_tr_b16 v[88:89], v97 offset:0
	ds_read_b64_tr_b16 v[90:91], v97 offset:0x800
	ds_read_b64_tr_b16 v[92:93], v97 offset:0x1000
	ds_read_b64_tr_b16 v[94:95], v97 offset:0x1800
	ds_read_b64_tr_b16 v[134:135], v97 offset:0x200
	ds_read_b64_tr_b16 v[136:137], v97 offset:0xa00
	ds_read_b64_tr_b16 v[138:139], v97 offset:0x1200
	ds_read_b64_tr_b16 v[140:141], v97 offset:0x1a00
	s_waitcnt lgkmcnt(0)
	s_nop 0
	v_permlane32_swap_b32_e32 v84, v86
	v_permlane32_swap_b32_e32 v85, v87
	v_permlane32_swap_b32_e32 v130, v132
	v_permlane32_swap_b32_e32 v131, v133
	s_nop 1
	v_mfma_f32_32x32x16_bf16 v[16:31], v[130:133], v[88:91], v[16:31]
	ds_read_b64_tr_b16 v[88:89], v97 offset:0x400
	ds_read_b64_tr_b16 v[90:91], v97 offset:0xc00
	v_mfma_f32_32x32x16_bf16 v[32:47], v[130:133], v[134:137], v[32:47]
	v_mfma_f32_32x32x16_bf16 v[16:31], v[84:87], v[92:95], v[16:31]
	ds_read_b64_tr_b16 v[92:93], v97 offset:0x1400
	ds_read_b64_tr_b16 v[94:95], v97 offset:0x1c00
	ds_read_b64_tr_b16 v[134:135], v97 offset:0x600
	ds_read_b64_tr_b16 v[136:137], v97 offset:0xe00
	v_mfma_f32_32x32x16_bf16 v[32:47], v[84:87], v[138:141], v[32:47]
	ds_read_b64_tr_b16 v[138:139], v97 offset:0x1600
	ds_read_b64_tr_b16 v[140:141], v97 offset:0x1e00
	s_waitcnt lgkmcnt(0)
	v_mfma_f32_32x32x16_bf16 v[48:63], v[130:133], v[88:91], v[48:63]
	v_mfma_f32_32x32x16_bf16 v[0:15], v[130:133], v[134:137], v[0:15]
	v_cvt_pk_bf16_f32 v134, v66, v67
	v_cvt_pk_bf16_f32 v135, v68, v69
	v_cvt_pk_bf16_f32 v136, v70, v82
	v_cvt_pk_bf16_f32 v137, v71, v73
	v_cvt_pk_bf16_f32 v130, v72, v74
	v_cvt_pk_bf16_f32 v131, v75, v76
	v_cvt_pk_bf16_f32 v132, v77, v78
	v_cvt_pk_bf16_f32 v133, v79, v80
	ds_read_b64_tr_b16 v[66:67], v97 offset:0x2000
	ds_read_b64_tr_b16 v[68:69], v97 offset:0x2800
	ds_read_b64_tr_b16 v[70:71], v97 offset:0x3000
	v_mfma_f32_32x32x16_bf16 v[48:63], v[84:87], v[92:95], v[48:63]
	ds_read_b64_tr_b16 v[72:73], v97 offset:0x3800
	ds_read_b64_tr_b16 v[74:75], v97 offset:0x2200
	ds_read_b64_tr_b16 v[76:77], v97 offset:0x2a00
	ds_read_b64_tr_b16 v[78:79], v97 offset:0x3200
	ds_read_b64_tr_b16 v[80:81], v97 offset:0x3a00
	s_waitcnt lgkmcnt(0)
	v_permlane32_swap_b32_e32 v134, v136
	v_mfma_f32_32x32x16_bf16 v[0:15], v[84:87], v[138:141], v[0:15]
	v_permlane32_swap_b32_e32 v135, v137
	v_permlane32_swap_b32_e32 v130, v132
	v_permlane32_swap_b32_e32 v131, v133
	v_mfma_f32_32x32x16_bf16 v[16:31], v[134:137], v[66:69], v[16:31]
	ds_read_b64_tr_b16 v[150:151], v97 offset:0x2400
	ds_read_b64_tr_b16 v[152:153], v97 offset:0x2c00
	ds_read_b64_tr_b16 v[142:143], v97 offset:0x3400
	ds_read_b64_tr_b16 v[144:145], v97 offset:0x3c00
	ds_read_b64_tr_b16 v[146:147], v97 offset:0x2600
	ds_read_b64_tr_b16 v[148:149], v97 offset:0x2e00
	ds_read_b64_tr_b16 v[138:139], v97 offset:0x3600
	v_mfma_f32_32x32x16_bf16 v[32:47], v[134:137], v[74:77], v[32:47]
	ds_read_b64_tr_b16 v[140:141], v97 offset:0x3e00
	s_waitcnt lgkmcnt(0)
	v_mfma_f32_32x32x16_bf16 v[16:31], v[130:133], v[70:73], v[16:31]
	v_mfma_f32_32x32x16_bf16 v[32:47], v[130:133], v[78:81], v[32:47]
	v_add_u32_e32 v175, s52, v168
	v_add_u32_e32 v86, v175, v169
	ds_read_b128 v[66:69], v86 offset:8192
	v_add_u32_e32 v176, v175, v162
	ds_read_b128 v[82:85], v176 offset:8192
	v_add_u32_e32 v180, v175, v163
	v_add_u32_e32 v181, v175, v164
	v_add_u32_e32 v182, v175, v165
	v_add_u32_e32 v183, v175, v166
	v_add_u32_e32 v184, v175, v167
	v_add_u32_e32 v175, v175, v161
	s_waitcnt lgkmcnt(1)
; #define LAS __attribute__((address_space(3)))
; template <int DK16, int DV32, bool MASK, int HALFWIN, bool RES, bool WT, class P>
; __device__ __forceinline__ void attn_unit(LAS unsigned char* lds, const P& c, const int ntiles, const float C, const int wv) {
;     ...
;                 for (int d0 = 0; d0 < DK16; ++d0) { const bf16x8 b0 = *(const LAS bf16x8*)(Ks + ATT_KSWZ(r32, (d0 * 16 + hi * 8) * 2)); p0 = __builtin_amdgcn_mfma_f32_32x32x16_bf16(b0, qr[d0], p0, 0, 0, 0); } }
;             if (do1) {
; #pragma unroll
;                 for (int d0 = 0; d0 < DK16; ++d0) { const bf16x8 b1 = *(const LAS bf16x8*)(Ks + ATT_KSWZ(32 + r32, (d0 * 16 + hi * 8) * 2)); p1 = __builtin_amdgcn_mfma_f32_32x32x16_bf16(b1, qr[d0], p1, 0, 0, 0); } }
;             if constexpr (MASK) {
;                 const int db = c.dbase(wid, r32, t) + 4 * hi, qi = c.qidx(wid, r32); const unsigned L = (unsigned)c.seqlen(); const bool edge = c.edge();
;                 const LAS float* tb = c.tab(wid) + (db + 2 * HALFWIN);
;     ...
;                 if (do0) ATT_XFORM(p0, 0);
;                 if (do1) ATT_XFORM(p1, 32);
;     ...
;             } else {
; #pragma unroll
;                 for (int r = 0; r < 16; ++r) { p0[r] *= C; p1[r] *= C; }
;             }
;             float pmax = -__builtin_inff();
;             if (do0) {
; #pragma unroll
;                 for (int r = 0; r < 16; ++r) pmax = fmaxf(pmax, p0[r]); }
;             if (do1) {
; #pragma unroll
;                 for (int r = 0; r < 16; ++r) pmax = fmaxf(pmax, p1[r]); }
;             { auto rr = __builtin_amdgcn_permlane32_swap(__float_as_uint(pmax), __float_as_uint(pmax), false, false);
;               pmax = fmaxf(__uint_as_float(rr[0]), __uint_as_float(rr[1])); }
;             const float mn = fmaxf(m_reg, pmax), alpha = __builtin_amdgcn_exp2f(m_reg - mn); m_reg = mn;
;             float ps = 0.f;
;             if (do0) {
; #pragma unroll
;                 for (int r = 0; r < 16; ++r) { p0[r] = __builtin_amdgcn_exp2f(p0[r] - mn); ps += p0[r]; } }
;             if (do1) {
; #pragma unroll
;                 for (int r = 0; r < 16; ++r) { p1[r] = __builtin_amdgcn_exp2f(p1[r] - mn); ps += p1[r]; } }
;             { auto rr = __builtin_amdgcn_permlane32_swap(__float_as_uint(ps), __float_as_uint(ps), false, false);
;               ps = __uint_as_float(rr[0]) + __uint_as_float(rr[1]); }
;             l_reg = l_reg * alpha + ps;
	v_mfma_f32_32x32x16_bf16 v[66:81], v[66:69], v[126:129], 0
	ds_read_b128 v[176:179], v176
	s_waitcnt lgkmcnt(1)
	v_mfma_f32_32x32x16_bf16 v[66:81], v[82:85], v[122:125], v[66:81]
	ds_read_b128 v[82:85], v180 offset:8192
	s_waitcnt lgkmcnt(0)
	v_mfma_f32_32x32x16_bf16 v[66:81], v[82:85], v[118:121], v[66:81]
	ds_read_b128 v[82:85], v181 offset:8192
	s_waitcnt lgkmcnt(0)
	v_mfma_f32_32x32x16_bf16 v[66:81], v[82:85], v[114:117], v[66:81]
	ds_read_b128 v[82:85], v182 offset:8192
	s_waitcnt lgkmcnt(0)
	v_mfma_f32_32x32x16_bf16 v[66:81], v[82:85], v[110:113], v[66:81]
	ds_read_b128 v[82:85], v183 offset:8192
	s_waitcnt lgkmcnt(0)
	v_mfma_f32_32x32x16_bf16 v[66:81], v[82:85], v[106:109], v[66:81]
	ds_read_b128 v[82:85], v184 offset:8192
	s_waitcnt lgkmcnt(0)
	v_mfma_f32_32x32x16_bf16 v[66:81], v[82:85], v[102:105], v[66:81]
	ds_read_b128 v[82:85], v86
	s_waitcnt lgkmcnt(0)
	v_mfma_f32_32x32x16_bf16 v[82:97], v[82:85], v[126:129], 0
	v_mfma_f32_32x32x16_bf16 v[82:97], v[176:179], v[122:125], v[82:97]
	ds_read_b128 v[176:179], v180
	s_waitcnt lgkmcnt(0)
	v_mfma_f32_32x32x16_bf16 v[82:97], v[176:179], v[118:121], v[82:97]
	ds_read_b128 v[176:179], v181
	s_waitcnt lgkmcnt(0)
	v_mfma_f32_32x32x16_bf16 v[82:97], v[176:179], v[114:117], v[82:97]
	ds_read_b128 v[176:179], v182
	s_waitcnt lgkmcnt(0)
	v_mfma_f32_32x32x16_bf16 v[82:97], v[176:179], v[110:113], v[82:97]
	ds_read_b128 v[176:179], v183
	s_waitcnt lgkmcnt(0)
	v_mfma_f32_32x32x16_bf16 v[82:97], v[176:179], v[106:109], v[82:97]
	ds_read_b128 v[176:179], v184
	s_waitcnt lgkmcnt(0)
	v_mfma_f32_32x32x16_bf16 v[82:97], v[176:179], v[102:105], v[82:97]
	ds_read_b128 v[176:179], v175
	s_waitcnt lgkmcnt(0)
	v_mfma_f32_32x32x16_bf16 v[82:97], v[176:179], v[98:101], v[82:97]
	ds_read_b128 v[176:179], v175 offset:8192
	s_waitcnt lgkmcnt(0)
	v_mfma_f32_32x32x16_bf16 v[66:81], v[176:179], v[98:101], v[66:81]
	s_nop 8
	v_mul_f32_e32 v175, 0x3e0293ee, v82
	v_mul_f32_e32 v177, 0x3e0293ee, v83
	v_mul_f32_e32 v179, 0x3e0293ee, v84
	v_mul_f32_e32 v181, 0x3e0293ee, v85
	v_max3_f32 v175, v175, s38, v177
	v_mul_f32_e32 v183, 0x3e0293ee, v86
	v_mul_f32_e32 v185, 0x3e0293ee, v87
	v_max3_f32 v175, v175, v179, v181
	v_mul_f32_e32 v187, 0x3e0293ee, v88
	v_mul_f32_e32 v189, 0x3e0293ee, v89
	v_max3_f32 v175, v175, v183, v185
	v_mul_f32_e32 v191, 0x3e0293ee, v90
	v_mul_f32_e32 v193, 0x3e0293ee, v91
	v_max3_f32 v175, v175, v187, v189
	v_mul_f32_e32 v195, 0x3e0293ee, v92
	v_mul_f32_e32 v197, 0x3e0293ee, v93
	v_max3_f32 v175, v175, v191, v193
	v_mul_f32_e32 v199, 0x3e0293ee, v94
	v_mul_f32_e32 v201, 0x3e0293ee, v95
	v_max3_f32 v175, v175, v195, v197
	v_mul_f32_e32 v203, 0x3e0293ee, v96
	v_mul_f32_e32 v205, 0x3e0293ee, v97
	v_max3_f32 v175, v175, v199, v201
	v_mul_f32_e32 v176, 0x3e0293ee, v66
	v_mul_f32_e32 v178, 0x3e0293ee, v67
	v_max3_f32 v175, v175, v203, v205
	v_mul_f32_e32 v180, 0x3e0293ee, v68
	v_mul_f32_e32 v182, 0x3e0293ee, v69
	v_max3_f32 v175, v175, v176, v178
	v_mul_f32_e32 v184, 0x3e0293ee, v70
	v_mul_f32_e32 v186, 0x3e0293ee, v71
	v_max3_f32 v175, v175, v180, v182
	v_mul_f32_e32 v188, 0x3e0293ee, v72
	v_mul_f32_e32 v190, 0x3e0293ee, v73
	v_max3_f32 v175, v175, v184, v186
	v_mul_f32_e32 v192, 0x3e0293ee, v74
	v_mul_f32_e32 v194, 0x3e0293ee, v75
	v_max3_f32 v175, v175, v188, v190
	v_mul_f32_e32 v196, 0x3e0293ee, v76
	v_mul_f32_e32 v198, 0x3e0293ee, v77
	v_max3_f32 v175, v175, v192, v194
	v_mul_f32_e32 v200, 0x3e0293ee, v78
	v_mul_f32_e32 v202, 0x3e0293ee, v79
	v_max3_f32 v175, v175, v196, v198
	v_mul_f32_e32 v204, 0x3e0293ee, v80
	v_mul_f32_e32 v206, 0x3e0293ee, v81
	v_max3_f32 v175, v175, v200, v202
	v_max3_f32 v175, v175, v204, v206
	v_mov_b32_e32 v176, v175
	s_nop 1
	v_permlane32_swap_b32_e32 v175, v176
	v_max3_f32 v177, v174, v175, v176
	v_sub_f32_e32 v176, v177, v174
	v_cmp_lt_f32_e32 vcc, 0x41000000, v176
	s_cbranch_vccnz .Llz_x2
	v_mov_b32_e32 v177, v174
.Llz_x2:
	v_fma_f32 v82, v82, s94, -v177
	v_exp_f32_e32 v178, v82
	v_fma_f32 v83, v83, s94, -v177
	v_exp_f32_e32 v83, v83
	v_fma_f32 v84, v84, s94, -v177
	v_exp_f32_e32 v84, v84
	v_fma_f32 v85, v85, s94, -v177
	v_exp_f32_e32 v85, v85
	v_fma_f32 v86, v86, s94, -v177
	v_add_f32_e32 v82, 0, v178
	v_exp_f32_e32 v86, v86
	v_fma_f32 v87, v87, s94, -v177
	v_add_f32_e32 v82, v83, v82
	v_exp_f32_e32 v179, v87
	v_fma_f32 v87, v88, s94, -v177
	v_add_f32_e32 v82, v84, v82
	v_exp_f32_e32 v88, v87
	v_fma_f32 v87, v89, s94, -v177
	v_add_f32_e32 v82, v85, v82
	v_exp_f32_e32 v89, v87
	v_fma_f32 v87, v90, s94, -v177
	v_add_f32_e32 v82, v86, v82
	v_exp_f32_e32 v87, v87
	v_fma_f32 v90, v91, s94, -v177
	v_add_f32_e32 v82, v179, v82
	v_exp_f32_e32 v90, v90
	v_fma_f32 v91, v92, s94, -v177
	v_add_f32_e32 v82, v88, v82
	v_exp_f32_e32 v91, v91
	v_fma_f32 v92, v93, s94, -v177
	v_add_f32_e32 v82, v89, v82
	v_exp_f32_e32 v92, v92
	v_fma_f32 v93, v94, s94, -v177
	v_add_f32_e32 v82, v87, v82
	v_exp_f32_e32 v93, v93
	v_fma_f32 v94, v95, s94, -v177
	v_add_f32_e32 v82, v90, v82
	v_exp_f32_e32 v94, v94
	v_fma_f32 v95, v96, s94, -v177
	v_add_f32_e32 v82, v91, v82
	v_exp_f32_e32 v95, v95
	v_fma_f32 v96, v97, s94, -v177
	v_add_f32_e32 v82, v92, v82
	v_exp_f32_e32 v96, v96
	v_fma_f32 v66, v66, s94, -v177
	v_add_f32_e32 v82, v93, v82
	v_exp_f32_e32 v66, v66
	v_fma_f32 v67, v67, s94, -v177
	v_add_f32_e32 v82, v94, v82
	v_exp_f32_e32 v67, v67
	v_fma_f32 v68, v68, s94, -v177
	v_add_f32_e32 v82, v95, v82
	v_exp_f32_e32 v68, v68
	v_fma_f32 v69, v69, s94, -v177
	v_add_f32_e32 v82, v96, v82
	v_exp_f32_e32 v69, v69
	v_add_f32_e32 v82, v66, v82
	v_add_f32_e32 v82, v67, v82
	v_fma_f32 v70, v70, s94, -v177
	v_add_f32_e32 v82, v68, v82
	v_exp_f32_e32 v70, v70
	v_fma_f32 v71, v71, s94, -v177
; __device__ __forceinline__ int crow(int r, int hi) { return (r & 3) + 8 * (r >> 2) + 4 * hi; }
; template <int DK16, int DV32, bool MASK, int HALFWIN, bool RES, bool WT, class P>
; __device__ __forceinline__ void attn_unit(LAS unsigned char* lds, const P& c, const int ntiles, const float C, const int wv) {
;     ...
;                 for (int r = 0; r < 16; ++r) { p0[r] = __builtin_amdgcn_exp2f(p0[r] - mn); ps += p0[r]; } }
;             if (do1) {
; #pragma unroll
;                 for (int r = 0; r < 16; ++r) { p1[r] = __builtin_amdgcn_exp2f(p1[r] - mn); ps += p1[r]; } }
;             { auto rr = __builtin_amdgcn_permlane32_swap(__float_as_uint(ps), __float_as_uint(ps), false, false);
;               ps = __uint_as_float(rr[0]) + __uint_as_float(rr[1]); }
;             l_reg = l_reg * alpha + ps;
;             if (__any(alpha < 1.f)) { if (hi == 0) al_l[r32] = alpha; asm volatile("s_waitcnt lgkmcnt(0)" ::: "memory");
; #pragma unroll
;                 for (int r = 0; r < 16; ++r) { const float a = al_l[crow(r, hi)];
; #pragma unroll
;                     for (int d = 0; d < DV32; ++d) o[d][r] *= a; } }
;             const int vb = vb0 + b * SHM_T;
;     ...
;             if (do0) { bf16x8 pa0, pa1; ATT_PK4(p0, 0, pa0); ATT_PK4(p0, 8, pa1);
;                 pv_half2<0, 1, 0>(o[0], o[1], vb, pa0, pa1);
;                 if constexpr (DV32 == 4) { pv_half2<2, 3, 0>(o[2], o[3], vb, pa0, pa1); } }
;             if (do1) { bf16x8 pa2, pa3; ATT_PK4(p1, 0, pa2); ATT_PK4(p1, 8, pa3);
;                 pv_half2<0, 1, 1>(o[0], o[1], vb, pa2, pa3);
;                 if constexpr (DV32 == 4) { pv_half2<2, 3, 1>(o[2], o[3], vb, pa2, pa3); } }
	v_add_f32_e32 v97, v69, v82
	v_exp_f32_e32 v82, v71
	v_fma_f32 v71, v72, s94, -v177
	v_exp_f32_e32 v71, v71
	v_fma_f32 v72, v73, s94, -v177
	v_exp_f32_e32 v73, v72
	v_add_f32_e32 v72, v70, v97
	v_add_f32_e32 v72, v82, v72
	v_add_f32_e32 v72, v71, v72
	v_add_f32_e32 v97, v73, v72
	v_fma_f32 v72, v74, s94, -v177
	v_exp_f32_e32 v72, v72
	v_fma_f32 v74, v75, s94, -v177
	v_exp_f32_e32 v74, v74
	v_fma_f32 v75, v76, s94, -v177
	v_mfma_f32_32x32x16_bf16 v[48:63], v[134:137], v[150:153], v[48:63]
	v_exp_f32_e32 v75, v75
	v_fma_f32 v76, v77, s94, -v177
	v_exp_f32_e32 v76, v76
	v_add_f32_e32 v77, v72, v97
	v_add_f32_e32 v77, v74, v77
	v_add_f32_e32 v77, v75, v77
	v_add_f32_e32 v97, v76, v77
	v_mfma_f32_32x32x16_bf16 v[0:15], v[134:137], v[146:149], v[0:15]
	v_fma_f32 v77, v78, s94, -v177
	v_exp_f32_e32 v77, v77
	v_fma_f32 v78, v79, s94, -v177
	v_exp_f32_e32 v78, v78
	v_fma_f32 v79, v80, s94, -v177
	v_exp_f32_e32 v79, v79
	v_fma_f32 v80, v81, s94, -v177
	v_mfma_f32_32x32x16_bf16 v[48:63], v[130:133], v[142:145], v[48:63]
	v_exp_f32_e32 v80, v80
	v_sub_f32_e32 v174, v174, v177
	v_add_f32_e32 v81, v77, v97
	v_add_f32_e32 v81, v78, v81
	v_exp_f32_e32 v174, v174
	v_add_f32_e32 v81, v79, v81
	v_add_f32_e32 v175, v80, v81
	v_mfma_f32_32x32x16_bf16 v[0:15], v[130:133], v[138:141], v[0:15]
	v_mov_b32_e32 v176, v175
	s_nop 1
	v_permlane32_swap_b32_e32 v175, v176
	v_cmp_gt_f32_e32 vcc, 1.0, v174
	s_cbranch_vccz .LBB0_1210
	v_cmp_gt_u32_e32 vcc, 32, v155
	s_and_saveexec_b64 s[0:1], vcc
	v_lshl_add_u32 v81, v156, 2, s10
	ds_write_b32 v81, v174 offset:128
	s_or_b64 exec, exec, s[0:1]
	s_waitcnt lgkmcnt(0)
	v_add_u32_e32 v81, s10, v64
	ds_read_b128 v[130:133], v81 offset:224
	ds_read_b128 v[134:137], v81 offset:192
	ds_read_b128 v[138:141], v81 offset:160
	ds_read_b128 v[142:145], v81 offset:128
	s_waitcnt lgkmcnt(3)
	v_pk_mul_f32 v[28:29], v[28:29], v[130:131]
	s_waitcnt lgkmcnt(2)
	v_pk_mul_f32 v[24:25], v[24:25], v[134:135]
	s_waitcnt lgkmcnt(1)
	v_pk_mul_f32 v[20:21], v[20:21], v[138:139]
	v_pk_mul_f32 v[30:31], v[30:31], v[132:133]
	v_pk_mul_f32 v[26:27], v[26:27], v[136:137]
	v_pk_mul_f32 v[22:23], v[22:23], v[140:141]
	s_waitcnt lgkmcnt(0)
	v_pk_mul_f32 v[18:19], v[18:19], v[144:145]
	v_pk_mul_f32 v[16:17], v[16:17], v[142:143]
	v_pk_mul_f32 v[44:45], v[44:45], v[130:131]
	v_pk_mul_f32 v[40:41], v[40:41], v[134:135]
	v_pk_mul_f32 v[36:37], v[36:37], v[138:139]
	v_pk_mul_f32 v[46:47], v[46:47], v[132:133]
	v_pk_mul_f32 v[42:43], v[42:43], v[136:137]
	v_pk_mul_f32 v[38:39], v[38:39], v[140:141]
	v_pk_mul_f32 v[34:35], v[34:35], v[144:145]
	v_pk_mul_f32 v[32:33], v[32:33], v[142:143]
	v_pk_mul_f32 v[60:61], v[60:61], v[130:131]
	v_pk_mul_f32 v[56:57], v[56:57], v[134:135]
	v_pk_mul_f32 v[52:53], v[52:53], v[138:139]
	v_pk_mul_f32 v[62:63], v[62:63], v[132:133]
	v_pk_mul_f32 v[58:59], v[58:59], v[136:137]
	v_pk_mul_f32 v[54:55], v[54:55], v[140:141]
	v_pk_mul_f32 v[50:51], v[50:51], v[144:145]
	v_pk_mul_f32 v[48:49], v[48:49], v[142:143]
	v_pk_mul_f32 v[12:13], v[12:13], v[130:131]
	v_pk_mul_f32 v[8:9], v[8:9], v[134:135]
	v_pk_mul_f32 v[4:5], v[4:5], v[138:139]
	v_pk_mul_f32 v[14:15], v[14:15], v[132:133]
	v_pk_mul_f32 v[10:11], v[10:11], v[136:137]
	v_pk_mul_f32 v[6:7], v[6:7], v[140:141]
	v_pk_mul_f32 v[2:3], v[2:3], v[144:145]
	v_pk_mul_f32 v[0:1], v[0:1], v[142:143]
.LBB0_1210:
	v_readlane_b32 s0, v254, 46
	v_cvt_pk_bf16_f32 v130, v178, v83
	v_cvt_pk_bf16_f32 v131, v84, v85
	v_cvt_pk_bf16_f32 v132, v86, v179
	v_cvt_pk_bf16_f32 v133, v88, v89
	v_cvt_pk_bf16_f32 v84, v87, v90
	s_nop 1
	v_add_u32_e32 v97, s0, v170
	v_cvt_pk_bf16_f32 v85, v91, v92
	v_cvt_pk_bf16_f32 v86, v93, v94
	v_cvt_pk_bf16_f32 v87, v95, v96
	ds_read_b64_tr_b16 v[88:89], v97 offset:0
	ds_read_b64_tr_b16 v[90:91], v97 offset:0x800
	ds_read_b64_tr_b16 v[92:93], v97 offset:0x1000
	ds_read_b64_tr_b16 v[94:95], v97 offset:0x1800
	ds_read_b64_tr_b16 v[134:135], v97 offset:0x200
	ds_read_b64_tr_b16 v[136:137], v97 offset:0xa00
	ds_read_b64_tr_b16 v[138:139], v97 offset:0x1200
	ds_read_b64_tr_b16 v[140:141], v97 offset:0x1a00
	s_waitcnt lgkmcnt(0)
	s_nop 0
	v_permlane32_swap_b32_e32 v84, v86
	v_permlane32_swap_b32_e32 v85, v87
	v_permlane32_swap_b32_e32 v130, v132
	v_permlane32_swap_b32_e32 v131, v133
	s_nop 1
	v_mfma_f32_32x32x16_bf16 v[16:31], v[130:133], v[88:91], v[16:31]
	ds_read_b64_tr_b16 v[88:89], v97 offset:0x400
	ds_read_b64_tr_b16 v[90:91], v97 offset:0xc00
	v_mfma_f32_32x32x16_bf16 v[32:47], v[130:133], v[134:137], v[32:47]
	v_mfma_f32_32x32x16_bf16 v[16:31], v[84:87], v[92:95], v[16:31]
	ds_read_b64_tr_b16 v[92:93], v97 offset:0x1400
	ds_read_b64_tr_b16 v[94:95], v97 offset:0x1c00
	ds_read_b64_tr_b16 v[134:135], v97 offset:0x600
	ds_read_b64_tr_b16 v[136:137], v97 offset:0xe00
	v_mfma_f32_32x32x16_bf16 v[32:47], v[84:87], v[138:141], v[32:47]
	ds_read_b64_tr_b16 v[138:139], v97 offset:0x1600
	ds_read_b64_tr_b16 v[140:141], v97 offset:0x1e00
	s_waitcnt lgkmcnt(0)
	v_mfma_f32_32x32x16_bf16 v[48:63], v[130:133], v[88:91], v[48:63]
	v_mfma_f32_32x32x16_bf16 v[0:15], v[130:133], v[134:137], v[0:15]
	v_cvt_pk_bf16_f32 v130, v66, v67
	v_cvt_pk_bf16_f32 v131, v68, v69
	v_cvt_pk_bf16_f32 v132, v70, v82
	v_cvt_pk_bf16_f32 v133, v71, v73
	v_cvt_pk_bf16_f32 v134, v72, v74
	v_cvt_pk_bf16_f32 v135, v75, v76
	v_cvt_pk_bf16_f32 v136, v77, v78
	v_cvt_pk_bf16_f32 v137, v79, v80
	ds_read_b64_tr_b16 v[66:67], v97 offset:0x2000
	ds_read_b64_tr_b16 v[68:69], v97 offset:0x2800
	ds_read_b64_tr_b16 v[70:71], v97 offset:0x3000
	v_mfma_f32_32x32x16_bf16 v[48:63], v[84:87], v[92:95], v[48:63]
	ds_read_b64_tr_b16 v[72:73], v97 offset:0x3800
	ds_read_b64_tr_b16 v[74:75], v97 offset:0x2200
	ds_read_b64_tr_b16 v[76:77], v97 offset:0x2a00
	ds_read_b64_tr_b16 v[78:79], v97 offset:0x3200
	ds_read_b64_tr_b16 v[80:81], v97 offset:0x3a00
	s_waitcnt lgkmcnt(0)
; #define LAS __attribute__((address_space(3)))
; template <int DK16, int DV32, bool MASK, int HALFWIN, bool RES, bool WT, class P>
; __device__ __forceinline__ void attn_unit(LAS unsigned char* lds, const P& c, const int ntiles, const float C, const int wv) {
;     ...
;             if (do0) {
; #pragma unroll
;                 for (int d0 = 0; d0 < DK16; ++d0) { const bf16x8 b0 = *(const LAS bf16x8*)(Ks + ATT_KSWZ(r32, (d0 * 16 + hi * 8) * 2)); p0 = __builtin_amdgcn_mfma_f32_32x32x16_bf16(b0, qr[d0], p0, 0, 0, 0); } }
;             if (do1) {
; #pragma unroll
;                 for (int d0 = 0; d0 < DK16; ++d0) { const bf16x8 b1 = *(const LAS bf16x8*)(Ks + ATT_KSWZ(32 + r32, (d0 * 16 + hi * 8) * 2)); p1 = __builtin_amdgcn_mfma_f32_32x32x16_bf16(b1, qr[d0], p1, 0, 0, 0); } }
;             if constexpr (MASK) {
;                 const int db = c.dbase(wid, r32, t) + 4 * hi, qi = c.qidx(wid, r32); const unsigned L = (unsigned)c.seqlen(); const bool edge = c.edge();
;                 const LAS float* tb = c.tab(wid) + (db + 2 * HALFWIN);
;     ...
;                 if (do0) ATT_XFORM(p0, 0);
;                 if (do1) ATT_XFORM(p1, 32);
;     ...
;             } else {
; #pragma unroll
;                 for (int r = 0; r < 16; ++r) { p0[r] *= C; p1[r] *= C; }
;             }
;             float pmax = -__builtin_inff();
;             if (do0) {
; #pragma unroll
;                 for (int r = 0; r < 16; ++r) pmax = fmaxf(pmax, p0[r]); }
;             if (do1) {
; #pragma unroll
;                 for (int r = 0; r < 16; ++r) pmax = fmaxf(pmax, p1[r]); }
;             { auto rr = __builtin_amdgcn_permlane32_swap(__float_as_uint(pmax), __float_as_uint(pmax), false, false);
;               pmax = fmaxf(__uint_as_float(rr[0]), __uint_as_float(rr[1])); }
;             const float mn = fmaxf(m_reg, pmax), alpha = __builtin_amdgcn_exp2f(m_reg - mn); m_reg = mn;
	v_permlane32_swap_b32_e32 v130, v132
	v_mfma_f32_32x32x16_bf16 v[0:15], v[84:87], v[138:141], v[0:15]
	v_permlane32_swap_b32_e32 v131, v133
	v_permlane32_swap_b32_e32 v134, v136
	v_permlane32_swap_b32_e32 v135, v137
	v_mfma_f32_32x32x16_bf16 v[16:31], v[130:133], v[66:69], v[16:31]
	ds_read_b64_tr_b16 v[150:151], v97 offset:0x2400
	ds_read_b64_tr_b16 v[152:153], v97 offset:0x2c00
	ds_read_b64_tr_b16 v[142:143], v97 offset:0x3400
	ds_read_b64_tr_b16 v[144:145], v97 offset:0x3c00
	ds_read_b64_tr_b16 v[146:147], v97 offset:0x2600
	ds_read_b64_tr_b16 v[148:149], v97 offset:0x2e00
	ds_read_b64_tr_b16 v[138:139], v97 offset:0x3600
	v_mfma_f32_32x32x16_bf16 v[32:47], v[130:133], v[74:77], v[32:47]
	ds_read_b64_tr_b16 v[140:141], v97 offset:0x3e00
	s_waitcnt lgkmcnt(0)
	v_mfma_f32_32x32x16_bf16 v[16:31], v[134:137], v[70:73], v[16:31]
	v_mfma_f32_32x32x16_bf16 v[32:47], v[134:137], v[78:81], v[32:47]
	v_add_u32_e32 v168, s53, v168
	v_add_u32_e32 v86, v168, v169
	ds_read_b128 v[66:69], v86 offset:8192
	v_add_u32_e32 v162, v168, v162
	ds_read_b128 v[82:85], v162 offset:8192
	v_add_u32_e32 v163, v168, v163
	v_add_u32_e32 v164, v168, v164
	v_add_u32_e32 v165, v168, v165
	v_add_u32_e32 v166, v168, v166
	v_add_u32_e32 v167, v168, v167
	v_mfma_f32_32x32x16_bf16 v[48:63], v[130:133], v[150:153], v[48:63]
	s_waitcnt lgkmcnt(1)
	v_mfma_f32_32x32x16_bf16 v[66:81], v[66:69], v[126:129], 0
	s_waitcnt lgkmcnt(0)
	v_mfma_f32_32x32x16_bf16 v[66:81], v[82:85], v[122:125], v[66:81]
	ds_read_b128 v[82:85], v163 offset:8192
	s_waitcnt lgkmcnt(0)
	v_mfma_f32_32x32x16_bf16 v[66:81], v[82:85], v[118:121], v[66:81]
	ds_read_b128 v[82:85], v164 offset:8192
	s_waitcnt lgkmcnt(0)
	v_mfma_f32_32x32x16_bf16 v[66:81], v[82:85], v[114:117], v[66:81]
	ds_read_b128 v[82:85], v165 offset:8192
	s_waitcnt lgkmcnt(0)
	v_mfma_f32_32x32x16_bf16 v[66:81], v[82:85], v[110:113], v[66:81]
	ds_read_b128 v[82:85], v166 offset:8192
	s_waitcnt lgkmcnt(0)
	v_mfma_f32_32x32x16_bf16 v[66:81], v[82:85], v[106:109], v[66:81]
	ds_read_b128 v[82:85], v167 offset:8192
	s_waitcnt lgkmcnt(0)
	v_mfma_f32_32x32x16_bf16 v[66:81], v[82:85], v[102:105], v[66:81]
	ds_read_b128 v[82:85], v86
	s_waitcnt lgkmcnt(0)
	v_mfma_f32_32x32x16_bf16 v[82:97], v[82:85], v[126:129], 0
	ds_read_b128 v[126:129], v162
	s_waitcnt lgkmcnt(0)
	v_mfma_f32_32x32x16_bf16 v[82:97], v[126:129], v[122:125], v[82:97]
	ds_read_b128 v[122:125], v163
	s_waitcnt lgkmcnt(0)
	v_mfma_f32_32x32x16_bf16 v[82:97], v[122:125], v[118:121], v[82:97]
	ds_read_b128 v[118:121], v164
	s_waitcnt lgkmcnt(0)
	v_mfma_f32_32x32x16_bf16 v[82:97], v[118:121], v[114:117], v[82:97]
	ds_read_b128 v[114:117], v165
	s_waitcnt lgkmcnt(0)
	v_mfma_f32_32x32x16_bf16 v[82:97], v[114:117], v[110:113], v[82:97]
	ds_read_b128 v[110:113], v166
	s_waitcnt lgkmcnt(0)
	v_mfma_f32_32x32x16_bf16 v[82:97], v[110:113], v[106:109], v[82:97]
	ds_read_b128 v[106:109], v167
	v_add_u32_e32 v110, v168, v161
	s_waitcnt lgkmcnt(0)
	v_mfma_f32_32x32x16_bf16 v[82:97], v[106:109], v[102:105], v[82:97]
	ds_read_b128 v[102:105], v110
	ds_read_b128 v[106:109], v110 offset:8192
	s_waitcnt lgkmcnt(1)
	v_mfma_f32_32x32x16_bf16 v[82:97], v[102:105], v[98:101], v[82:97]
	s_waitcnt lgkmcnt(0)
	v_mfma_f32_32x32x16_bf16 v[66:81], v[106:109], v[98:101], v[66:81]
	s_nop 9
	v_mul_f32_e32 v102, 0x3e0293ee, v82
	v_mul_f32_e32 v99, 0x3e0293ee, v83
	v_mul_f32_e32 v101, 0x3e0293ee, v84
	v_mul_f32_e32 v104, 0x3e0293ee, v85
	v_max3_f32 v99, v102, s38, v99
	v_mul_f32_e32 v106, 0x3e0293ee, v86
	v_mul_f32_e32 v108, 0x3e0293ee, v87
	v_max3_f32 v99, v99, v101, v104
	v_mul_f32_e32 v110, 0x3e0293ee, v88
	v_mul_f32_e32 v112, 0x3e0293ee, v89
	v_max3_f32 v99, v99, v106, v108
	v_mul_f32_e32 v114, 0x3e0293ee, v90
	v_mul_f32_e32 v116, 0x3e0293ee, v91
	v_max3_f32 v99, v99, v110, v112
	v_mul_f32_e32 v118, 0x3e0293ee, v92
	v_mul_f32_e32 v120, 0x3e0293ee, v93
	v_max3_f32 v99, v99, v114, v116
	v_mul_f32_e32 v122, 0x3e0293ee, v94
	v_mul_f32_e32 v124, 0x3e0293ee, v95
	v_max3_f32 v99, v99, v118, v120
	v_mul_f32_e32 v126, 0x3e0293ee, v96
	v_mul_f32_e32 v128, 0x3e0293ee, v97
	v_max3_f32 v99, v99, v122, v124
	v_mul_f32_e32 v98, 0x3e0293ee, v66
	v_mul_f32_e32 v100, 0x3e0293ee, v67
	v_max3_f32 v99, v99, v126, v128
	v_mul_f32_e32 v103, 0x3e0293ee, v68
	v_mul_f32_e32 v105, 0x3e0293ee, v69
	v_max3_f32 v98, v99, v98, v100
	v_mul_f32_e32 v107, 0x3e0293ee, v70
	v_mul_f32_e32 v109, 0x3e0293ee, v71
	v_max3_f32 v98, v98, v103, v105
	v_mul_f32_e32 v111, 0x3e0293ee, v72
	v_mul_f32_e32 v113, 0x3e0293ee, v73
	v_max3_f32 v98, v98, v107, v109
	v_mul_f32_e32 v115, 0x3e0293ee, v74
	v_mul_f32_e32 v117, 0x3e0293ee, v75
	v_max3_f32 v98, v98, v111, v113
	v_mul_f32_e32 v119, 0x3e0293ee, v76
	v_mul_f32_e32 v121, 0x3e0293ee, v77
	v_max3_f32 v98, v98, v115, v117
	v_mul_f32_e32 v123, 0x3e0293ee, v78
	v_mul_f32_e32 v125, 0x3e0293ee, v79
	v_max3_f32 v98, v98, v119, v121
	v_mul_f32_e32 v127, 0x3e0293ee, v80
	v_mul_f32_e32 v129, 0x3e0293ee, v81
	v_max3_f32 v98, v98, v123, v125
	v_max3_f32 v98, v98, v127, v129
	v_mov_b32_e32 v99, v98
	s_nop 1
	v_permlane32_swap_b32_e32 v98, v99
	v_max3_f32 v106, v177, v98, v99
	v_sub_f32_e32 v99, v106, v177
	v_cmp_lt_f32_e32 vcc, 0x41000000, v99
	s_cbranch_vccnz .Llz_x3
	v_mov_b32_e32 v106, v177
; __device__ __forceinline__ int crow(int r, int hi) { return (r & 3) + 8 * (r >> 2) + 4 * hi; }
; template <int DK16, int DV32, bool MASK, int HALFWIN, bool RES, bool WT, class P>
; __device__ __forceinline__ void attn_unit(LAS unsigned char* lds, const P& c, const int ntiles, const float C, const int wv) {
;     ...
;             const float mn = fmaxf(m_reg, pmax), alpha = __builtin_amdgcn_exp2f(m_reg - mn); m_reg = mn;
;             float ps = 0.f;
;             if (do0) {
; #pragma unroll
;                 for (int r = 0; r < 16; ++r) { p0[r] = __builtin_amdgcn_exp2f(p0[r] - mn); ps += p0[r]; } }
;             if (do1) {
; #pragma unroll
;                 for (int r = 0; r < 16; ++r) { p1[r] = __builtin_amdgcn_exp2f(p1[r] - mn); ps += p1[r]; } }
;             { auto rr = __builtin_amdgcn_permlane32_swap(__float_as_uint(ps), __float_as_uint(ps), false, false);
;               ps = __uint_as_float(rr[0]) + __uint_as_float(rr[1]); }
;             l_reg = l_reg * alpha + ps;
;             if (__any(alpha < 1.f)) { if (hi == 0) al_l[r32] = alpha; asm volatile("s_waitcnt lgkmcnt(0)" ::: "memory");
; #pragma unroll
;                 for (int r = 0; r < 16; ++r) { const float a = al_l[crow(r, hi)];
; #pragma unroll
;                     for (int d = 0; d < DV32; ++d) o[d][r] *= a; } }
.Llz_x3:
	v_fma_f32 v82, v82, s94, -v106
	v_exp_f32_e32 v98, v82
	v_fma_f32 v83, v83, s94, -v106
	v_exp_f32_e32 v99, v83
	v_fma_f32 v83, v84, s94, -v106
	v_exp_f32_e32 v100, v83
	v_fma_f32 v83, v85, s94, -v106
	v_exp_f32_e32 v101, v83
	v_fma_f32 v83, v86, s94, -v106
	v_add_f32_e32 v82, 0, v98
	v_exp_f32_e32 v102, v83
	v_fma_f32 v83, v87, s94, -v106
	v_add_f32_e32 v82, v99, v82
	v_exp_f32_e32 v103, v83
	v_fma_f32 v83, v88, s94, -v106
	v_add_f32_e32 v82, v100, v82
	v_exp_f32_e32 v104, v83
	v_fma_f32 v83, v89, s94, -v106
	v_add_f32_e32 v82, v101, v82
	v_exp_f32_e32 v105, v83
	v_fma_f32 v83, v90, s94, -v106
	v_add_f32_e32 v82, v102, v82
	v_exp_f32_e32 v89, v83
	v_fma_f32 v83, v91, s94, -v106
	v_add_f32_e32 v82, v103, v82
	v_exp_f32_e32 v90, v83
	v_fma_f32 v83, v92, s94, -v106
	v_add_f32_e32 v82, v104, v82
	v_exp_f32_e32 v91, v83
	v_fma_f32 v83, v93, s94, -v106
	v_add_f32_e32 v82, v105, v82
	v_exp_f32_e32 v92, v83
	v_fma_f32 v83, v94, s94, -v106
	v_add_f32_e32 v82, v89, v82
	v_exp_f32_e32 v93, v83
	v_fma_f32 v83, v95, s94, -v106
	v_add_f32_e32 v82, v90, v82
	v_exp_f32_e32 v94, v83
	v_fma_f32 v83, v96, s94, -v106
	v_add_f32_e32 v82, v91, v82
	v_exp_f32_e32 v95, v83
	v_fma_f32 v83, v97, s94, -v106
	v_add_f32_e32 v82, v92, v82
	v_exp_f32_e32 v96, v83
	v_add_f32_e32 v82, v93, v82
	v_add_f32_e32 v82, v94, v82
	v_add_f32_e32 v82, v95, v82
	v_fma_f32 v66, v66, s94, -v106
	v_add_f32_e32 v86, v96, v82
	v_exp_f32_e32 v82, v66
	v_fma_f32 v66, v67, s94, -v106
	v_exp_f32_e32 v83, v66
	v_fma_f32 v66, v68, s94, -v106
	v_exp_f32_e32 v84, v66
	v_fma_f32 v66, v69, s94, -v106
	v_exp_f32_e32 v85, v66
	v_fma_f32 v67, v70, s94, -v106
	v_add_f32_e32 v66, v82, v86
	v_exp_f32_e32 v86, v67
	v_fma_f32 v67, v71, s94, -v106
	v_add_f32_e32 v66, v83, v66
	v_exp_f32_e32 v88, v67
	v_fma_f32 v67, v72, s94, -v106
	v_add_f32_e32 v66, v84, v66
	v_exp_f32_e32 v72, v67
	v_fma_f32 v67, v73, s94, -v106
	v_add_f32_e32 v66, v85, v66
	v_exp_f32_e32 v87, v67
	v_fma_f32 v67, v74, s94, -v106
	v_mfma_f32_32x32x16_bf16 v[0:15], v[130:133], v[146:149], v[0:15]
	v_add_f32_e32 v66, v86, v66
	v_exp_f32_e32 v69, v67
	v_fma_f32 v67, v75, s94, -v106
	v_add_f32_e32 v66, v88, v66
	v_exp_f32_e32 v70, v67
	v_fma_f32 v67, v76, s94, -v106
	v_add_f32_e32 v66, v72, v66
	v_exp_f32_e32 v71, v67
	v_fma_f32 v67, v77, s94, -v106
	v_add_f32_e32 v66, v87, v66
	v_exp_f32_e32 v74, v67
	v_fma_f32 v67, v78, s94, -v106
	v_add_f32_e32 v66, v69, v66
	v_exp_f32_e32 v73, v67
	v_fma_f32 v67, v79, s94, -v106
	v_add_f32_e32 v66, v70, v66
	v_exp_f32_e32 v75, v67
	v_fma_f32 v67, v80, s94, -v106
	v_add_f32_e32 v66, v71, v66
	v_exp_f32_e32 v76, v67
	v_fma_f32 v67, v81, s94, -v106
	v_add_f32_e32 v66, v74, v66
	v_exp_f32_e32 v77, v67
	v_mfma_f32_32x32x16_bf16 v[48:63], v[134:137], v[142:145], v[48:63]
	v_add_f32_e32 v66, v73, v66
	v_add_f32_e32 v66, v75, v66
	v_sub_f32_e32 v107, v177, v106
	v_add_f32_e32 v66, v76, v66
	v_add_f32_e32 v67, v77, v66
	v_exp_f32_e32 v66, v107
	v_mov_b32_e32 v68, v67
	v_mfma_f32_32x32x16_bf16 v[0:15], v[134:137], v[138:141], v[0:15]
	s_nop 0
	v_permlane32_swap_b32_e32 v67, v68
	v_cmp_gt_f32_e32 vcc, 1.0, v66
	s_cbranch_vccz .LBB0_1214
	v_cmp_gt_u32_e32 vcc, 32, v155
	s_and_saveexec_b64 s[0:1], vcc
	v_lshl_add_u32 v78, v156, 2, s10
	ds_write_b32 v78, v66 offset:128
	s_or_b64 exec, exec, s[0:1]
	s_waitcnt lgkmcnt(0)
	v_add_u32_e32 v64, s10, v64
	ds_read_b128 v[78:81], v64 offset:224
	ds_read_b128 v[106:109], v64 offset:192
	ds_read_b128 v[110:113], v64 offset:160
	ds_read_b128 v[114:117], v64 offset:128
	s_waitcnt lgkmcnt(3)
	v_pk_mul_f32 v[28:29], v[28:29], v[78:79]
	s_waitcnt lgkmcnt(2)
	v_pk_mul_f32 v[24:25], v[24:25], v[106:107]
	s_waitcnt lgkmcnt(1)
	v_pk_mul_f32 v[20:21], v[20:21], v[110:111]
	v_pk_mul_f32 v[30:31], v[30:31], v[80:81]
	v_pk_mul_f32 v[26:27], v[26:27], v[108:109]
	v_pk_mul_f32 v[22:23], v[22:23], v[112:113]
	s_waitcnt lgkmcnt(0)
	v_pk_mul_f32 v[18:19], v[18:19], v[116:117]
	v_pk_mul_f32 v[16:17], v[16:17], v[114:115]
	v_pk_mul_f32 v[44:45], v[44:45], v[78:79]
	v_pk_mul_f32 v[40:41], v[40:41], v[106:107]
	v_pk_mul_f32 v[36:37], v[36:37], v[110:111]
	v_pk_mul_f32 v[46:47], v[46:47], v[80:81]
	v_pk_mul_f32 v[42:43], v[42:43], v[108:109]
	v_pk_mul_f32 v[38:39], v[38:39], v[112:113]
	v_pk_mul_f32 v[34:35], v[34:35], v[116:117]
	v_pk_mul_f32 v[32:33], v[32:33], v[114:115]
	v_pk_mul_f32 v[60:61], v[60:61], v[78:79]
	v_pk_mul_f32 v[56:57], v[56:57], v[106:107]
	v_pk_mul_f32 v[52:53], v[52:53], v[110:111]
	v_pk_mul_f32 v[62:63], v[62:63], v[80:81]
	v_pk_mul_f32 v[58:59], v[58:59], v[108:109]
	v_pk_mul_f32 v[54:55], v[54:55], v[112:113]
	v_pk_mul_f32 v[50:51], v[50:51], v[116:117]
	v_pk_mul_f32 v[48:49], v[48:49], v[114:115]
	v_pk_mul_f32 v[12:13], v[12:13], v[78:79]
	v_pk_mul_f32 v[8:9], v[8:9], v[106:107]
	v_pk_mul_f32 v[4:5], v[4:5], v[110:111]
	v_pk_mul_f32 v[14:15], v[14:15], v[80:81]
	v_pk_mul_f32 v[10:11], v[10:11], v[108:109]
	v_pk_mul_f32 v[6:7], v[6:7], v[112:113]
	v_pk_mul_f32 v[2:3], v[2:3], v[116:117]
	v_pk_mul_f32 v[0:1], v[0:1], v[114:115]
